# grid barrier rewritten by hand: arrival add + early invalidate, XCD-last does write-back and adds on TOP, all poll TOP (no TOPGEN/XGEN hops, no divisions)
# speedup vs baseline: 1.0208x; 1.0150x over previous
; __device__ __forceinline__ unsigned xb_ld(unsigned* p)              { return __hip_atomic_load(p, __ATOMIC_RELAXED, __HIP_MEMORY_SCOPE_AGENT); }
; __device__ __forceinline__ unsigned xb_add(unsigned* p, unsigned v) { return __hip_atomic_fetch_add(p, v, __ATOMIC_RELAXED, __HIP_MEMORY_SCOPE_AGENT); }
; #define XB_SPIN(cond, bar) do { unsigned _sp = 0; while (cond) { __builtin_amdgcn_s_sleep(1); \
;     if ((++_sp & 255u) == 0u) { if (xb_ld(&(bar)[XB_TMO])) break; if (_sp > XB_SPIN_CAP) { atomicAdd(&(bar)[XB_TMO], 1u); break; } } } } while (0)
; __device__ __forceinline__ void xcd_barrier(const XcdBarrier& b) {
;     asm volatile("s_waitcnt vmcnt(0)" ::: "memory");
;     __syncthreads();
;     if (threadIdx.x == 0) {
;         unsigned* bar = b.bar;
;         __builtin_amdgcn_s_waitcnt(0);
;         unsigned nloc = b.st[0], nx = b.st[1];
;         if (nloc == 0u) { xcd_barrier_complete(bar, b.x, nloc, nx); b.st[0] = nloc; b.st[1] = nx; }
;         const unsigned old = xb_add(&bar[XB_XSUB(b.x)], 1u);
;         const unsigned gen = old / nloc;
;         if (old + 1u == (gen + 1u) * nloc) {
;             __builtin_amdgcn_fence(__ATOMIC_RELEASE, "agent");
;             asm volatile("s_waitcnt vmcnt(0)" ::: "memory");
;             const unsigned og = xb_add(&bar[XB_TOP], 1u);
;             const unsigned tg = og / nx;
;             if (og + 1u == (tg + 1u) * nx) xb_add(&bar[XB_TOPGEN], 1u);
;             else XB_SPIN(xb_ld(&bar[XB_TOPGEN]) == tg, bar);
;             __builtin_amdgcn_fence(__ATOMIC_ACQUIRE, "agent");
;             xb_add(&bar[XB_XGEN(b.x)], 1u);
;             asm volatile("s_waitcnt vmcnt(0)" ::: "memory");
;         } else {
;             XB_SPIN(xb_ld(&bar[XB_XGEN(b.x)]) == gen, bar);
;             __builtin_amdgcn_fence(__ATOMIC_ACQUIRE, "agent");
;             asm volatile("s_waitcnt vmcnt(0)" ::: "memory");
;         }
.LBB0_111:
	s_lshl_b32 s4, s33, 8
	s_add_u32 s4, s84, s4
	s_addc_u32 s5, s85, 0
	v_mov_b32_e32 v2, 0x20800
	ds_read_b32 v6, v2 offset:8
	v_mov_b32_e32 v4, 0x1400
	v_mov_b32_e32 v5, 1
	global_atomic_add v4, v4, v5, s[4:5] sc0
	buffer_inv sc1
	s_waitcnt vmcnt(1) lgkmcnt(0)
	v_readfirstlane_b32 s6, v3
	v_readfirstlane_b32 s7, v1
	v_readfirstlane_b32 s8, v6
	v_readfirstlane_b32 s9, v4
	s_add_u32 s8, s8, 1
	v_mov_b32_e32 v6, s8
	ds_write_b32 v2, v6 offset:8
	s_mul_i32 s6, s6, s8
	s_mul_i32 s7, s7, s8
	s_add_u32 s9, s9, 1
	v_mov_b32_e32 v4, 0x3400
	s_cmp_lg_u32 s9, s6
	s_cbranch_scc1 .Lxb1_poll0
	buffer_wbl2 sc1
	s_waitcnt vmcnt(0)
	global_atomic_add v4, v5, s[84:85]
.Lxb1_poll0:
	s_mov_b32 s6, 0
.Lxb1_poll:
	global_load_dword v3, v4, s[84:85] sc1
	s_waitcnt vmcnt(0)
	v_readfirstlane_b32 s9, v3
	s_cmp_ge_u32 s9, s7
	s_cbranch_scc1 .Lxb1_done
	s_sleep 1
	s_add_u32 s6, s6, 1
	s_cmp_lt_u32 s6, 0x400000
	s_cbranch_scc1 .Lxb1_poll
.Lxb1_done:
	s_waitcnt vmcnt(0) lgkmcnt(0)

; __device__ __forceinline__ unsigned xb_ld(unsigned* p)              { return __hip_atomic_load(p, __ATOMIC_RELAXED, __HIP_MEMORY_SCOPE_AGENT); }
; __device__ __forceinline__ unsigned xb_add(unsigned* p, unsigned v) { return __hip_atomic_fetch_add(p, v, __ATOMIC_RELAXED, __HIP_MEMORY_SCOPE_AGENT); }
; #define XB_SPIN(cond, bar) do { unsigned _sp = 0; while (cond) { __builtin_amdgcn_s_sleep(1); \
;     if ((++_sp & 255u) == 0u) { if (xb_ld(&(bar)[XB_TMO])) break; if (_sp > XB_SPIN_CAP) { atomicAdd(&(bar)[XB_TMO], 1u); break; } } } } while (0)
; __device__ __forceinline__ void xcd_barrier(const XcdBarrier& b) {
;     asm volatile("s_waitcnt vmcnt(0)" ::: "memory");
;     __syncthreads();
;     if (threadIdx.x == 0) {
;         unsigned* bar = b.bar;
;         __builtin_amdgcn_s_waitcnt(0);
;         unsigned nloc = b.st[0], nx = b.st[1];
;         if (nloc == 0u) { xcd_barrier_complete(bar, b.x, nloc, nx); b.st[0] = nloc; b.st[1] = nx; }
;         const unsigned old = xb_add(&bar[XB_XSUB(b.x)], 1u);
;         const unsigned gen = old / nloc;
;         if (old + 1u == (gen + 1u) * nloc) {
;             __builtin_amdgcn_fence(__ATOMIC_RELEASE, "agent");
;             asm volatile("s_waitcnt vmcnt(0)" ::: "memory");
;             const unsigned og = xb_add(&bar[XB_TOP], 1u);
;             const unsigned tg = og / nx;
;             if (og + 1u == (tg + 1u) * nx) xb_add(&bar[XB_TOPGEN], 1u);
;             else XB_SPIN(xb_ld(&bar[XB_TOPGEN]) == tg, bar);
;             __builtin_amdgcn_fence(__ATOMIC_ACQUIRE, "agent");
;             xb_add(&bar[XB_XGEN(b.x)], 1u);
;             asm volatile("s_waitcnt vmcnt(0)" ::: "memory");
;         } else {
;             XB_SPIN(xb_ld(&bar[XB_XGEN(b.x)]) == gen, bar);
;             __builtin_amdgcn_fence(__ATOMIC_ACQUIRE, "agent");
;             asm volatile("s_waitcnt vmcnt(0)" ::: "memory");
;         }
.LBB0_169:
	s_lshl_b32 s2, s33, 8
	s_add_u32 s2, s84, s2
	s_addc_u32 s3, s85, 0
	v_mov_b32_e32 v2, 0x20800
	ds_read_b32 v6, v2 offset:8
	v_mov_b32_e32 v4, 0x1400
	v_mov_b32_e32 v5, 1
	global_atomic_add v4, v4, v5, s[2:3] sc0
	buffer_inv sc1
	s_waitcnt vmcnt(1) lgkmcnt(0)
	v_readfirstlane_b32 s4, v3
	v_readfirstlane_b32 s5, v1
	v_readfirstlane_b32 s6, v6
	v_readfirstlane_b32 s7, v4
	s_add_u32 s6, s6, 1
	v_mov_b32_e32 v6, s6
	ds_write_b32 v2, v6 offset:8
	s_mul_i32 s4, s4, s6
	s_mul_i32 s5, s5, s6
	s_add_u32 s7, s7, 1
	v_mov_b32_e32 v4, 0x3400
	s_cmp_lg_u32 s7, s4
	s_cbranch_scc1 .Lxb2_poll0
	buffer_wbl2 sc1
	s_waitcnt vmcnt(0)
	global_atomic_add v4, v5, s[84:85]
.Lxb2_poll0:
	s_mov_b32 s4, 0
.Lxb2_poll:
	global_load_dword v3, v4, s[84:85] sc1
	s_waitcnt vmcnt(0)
	v_readfirstlane_b32 s7, v3
	s_cmp_ge_u32 s7, s5
	s_cbranch_scc1 .Lxb2_done
	s_sleep 1
	s_add_u32 s4, s4, 1
	s_cmp_lt_u32 s4, 0x400000
	s_cbranch_scc1 .Lxb2_poll

; __global__ void __launch_bounds__(512, 2) fwd(Params p) {
;     ...
;     for (int l = 0; l < 2; ++l) {
;         const int pb = 2 + NPH_LAYER * l;
;         const float* mod = (const float*)(ws + WS_MOD) + (size_t)l * 5 * 12288;
;         if (PSEL(2) && IN(pb + 0)) REPLOOP(2) {
;             pg8::EpiStoreBf16 E{(bf16_t*)(ws + WS_PA), INP};
;             if (l == 0) { if (c >= GgA) moe_convert_while(p, lds, pb + 0, GgA);
;                 else { pg8::TileSched S; S.init(ws + WS_H, (bf16_t*)(ws + WS_WTIN), DM, DM, MT / 256, INP / 256, 1, 0, 0, GgA, c, 0); pg8::gemm_phase(lds, pg8::Desc{DM, DM, DM}, S, E); if (nconv) moe_mark_done(p, pb + 0); } }
;             else { pg8::InSchedLast S; S.init(ws + WS_H, (bf16_t*)(ws + WS_WTIN) + (size_t)INP * DM, G, c); pg8::gemm_phase(lds, pg8::Desc{DM, DM, DM}, S, E); }
;             moe_fill(p, lds, pb + 0);
;          REPBAR(2); }
;         SEAM(pb + 0);
;         if (PSEL(3) && IN(pb + 1)) REPLOOP(3) { ph_rowsplit(p, l, lds); __syncthreads();  REPBAR(3); }
;         SEAM(pb + 1);
;         if (PSEL(4) && IN(pb + 2)) REPLOOP(4) {
;     ...
;             if (C_SEL & 1) { pg8::TileSched S; S.init(ws + WS_QA, (bf16_t*)(ws + WS_WTUQ) + (size_t)l * 768 * 384, 384, 384, (l == 0 ? MT : NLAT) / 256, 3, 1, 0, 0, G, c, 0);
;               pg8::EpiQ E{(bf16_t*)(ws + WS_QB), (const f32x2*)(ws + WS_ROPE)}; pg8::gemm_phase(lds, pg8::Desc{384, 384, 384}, S, E); }
;             if (C_SEL & 2) { pg8::TileSched S; S.init(ws + WS_KVA, (bf16_t*)(ws + WS_WTUKV) + (size_t)l * 1024 * 256, 256, 256, MT / 256, 2, 1, 0, 0, G, c, 112);
;               pg8::EpiK E{(bf16_t*)(ws + WS_KC)}; pg8::gemm_phase(lds, pg8::Desc{256, 256, 256}, S, E); }
;             if (C_SEL & 4) { pg8::TileSched S; S.init((bf16_t*)(ws + WS_WTUKV) + (size_t)l * 1024 * 256 + 512 * 256, ws + WS_KVA, 256, 256, 2, MT / 256, 1, 0, 0, G, c, 184);
;               pg8::EpiV E{(bf16_t*)(ws + WS_VT)}; pg8::gemm_phase(lds, pg8::Desc{256, 256, 256}, S, E); }
;             if (C_SEL & 8) { pg8::TileSched S; S.init(ws + WS_UPK, (bf16_t*)(ws + WS_WST) + (size_t)l * 32 * 256 * 256, 512, 256, 3, 1, 32, (size_t)768 * 512 * 2, (size_t)256 * 256 * 2, G, c, G == 256 ? 112 : 0);
;               pg8::EpiS1 E{(float*)(ws + WS_EST)}; pg8::gemm_phase(lds, pg8::Desc{512, 256, 256}, S, E); }
;             if (G == 256) { const int j = c < 112 ? c : (c >= 208 ? 112 + (c - 208) : -1);
.LBB0_202:
	v_readlane_b32 s24, v251, 50
	v_readlane_b32 s25, v251, 51
	s_and_b64 s[0:1], s[24:25], exec
	s_cselect_b32 s0, 0xffffffb8, 0
	s_add_i32 s26, s0, s94
	s_and_b64 s[0:1], s[24:25], exec
	s_cselect_b32 s0, 0xffffff90, 0
	s_add_i32 s4, s0, s94
	s_and_b64 s[0:1], s[24:25], exec
	s_cselect_b32 s0, 0xffffffd8, 0
	s_add_i32 s7, s0, s94
	s_add_u32 s0, s84, 0x1f1b8000
	s_addc_u32 s1, s85, 0
	v_writelane_b32 v252, s0, 22
	v_readlane_b32 s8, v251, 16
	v_readlane_b32 s9, v251, 17
	v_writelane_b32 v252, s1, 23
	s_add_u32 s0, s84, 0x1cdb8000
	s_addc_u32 s1, s85, 0
	v_writelane_b32 v252, s0, 24
	v_readlane_b32 s10, v251, 18
	v_readlane_b32 s11, v251, 19
	v_writelane_b32 v252, s1, 25
	s_add_u32 s0, s84, 0xf88000
	v_writelane_b32 v252, s0, 26
	s_addc_u32 s0, s85, 0
	v_writelane_b32 v252, s0, 27
	s_add_i32 s27, s94, s92
	s_ashr_i32 s0, s94, 31
	s_cmp_ge_i32 s92, s26
	v_writelane_b32 v252, s0, 0
	s_cselect_b64 s[0:1], -1, 0
	v_writelane_b32 v252, s0, 28
	s_cmp_eq_u32 s26, 0
	v_readlane_b32 s12, v251, 20
	v_writelane_b32 v252, s1, 29
	s_cselect_b32 s0, s94, s26
	v_writelane_b32 v252, s0, 30
	s_add_u32 s0, s84, 0x88000
	v_writelane_b32 v252, s0, 31
	s_addc_u32 s0, s85, 0
	v_writelane_b32 v252, s0, 32
	s_ashr_i32 s0, s26, 31
	v_writelane_b32 v252, s0, 33
	v_cmp_eq_u32_e64 s[0:1], 0, v0
	s_add_i32 s6, s26, s92
	v_readlane_b32 s13, v251, 21
	v_writelane_b32 v252, s0, 34
	v_readlane_b32 s14, v251, 22
	v_readlane_b32 s15, v251, 23
	v_writelane_b32 v252, s1, 35
	s_and_b64 s[0:1], s[0:1], s[24:25]
	v_writelane_b32 v252, s0, 36
	v_readlane_b32 s16, v251, 24
	v_readlane_b32 s17, v251, 25
	v_writelane_b32 v252, s1, 37
	s_add_u32 s0, s84, 0x4300
	s_addc_u32 s1, s85, 0
	v_writelane_b32 v252, s0, 38
	v_readlane_b32 s18, v251, 26
	v_readlane_b32 s19, v251, 27
	v_writelane_b32 v252, s1, 39
	s_add_u32 s0, s84, 0x200
	s_addc_u32 s1, s85, 0
	v_writelane_b32 v252, s0, 40
	s_mov_b64 s[8:9], s[12:13]
	v_readlane_b32 s20, v251, 28
	v_writelane_b32 v252, s1, 41
	s_add_u32 s0, s84, 0x1000
	s_addc_u32 s1, s85, 0
	v_writelane_b32 v252, s0, 18
	v_readlane_b32 s21, v251, 29
	v_readlane_b32 s22, v251, 30
	v_writelane_b32 v252, s1, 19
	s_add_u32 s0, s84, 0x1100
	s_addc_u32 s1, s85, 0
	v_writelane_b32 v252, s0, 13
	v_readlane_b32 s23, v251, 31
	s_mov_b64 s[10:11], s[14:15]
	v_writelane_b32 v252, s1, 14
	s_add_u32 s0, s84, 0x1200
	s_addc_u32 s1, s85, 0
	v_writelane_b32 v252, s0, 15
	s_mov_b64 s[12:13], s[16:17]
	s_mov_b64 s[14:15], s[18:19]
	v_writelane_b32 v252, s1, 16
	s_add_u32 s0, s84, 0x1300
	s_addc_u32 s1, s85, 0
	v_writelane_b32 v252, s0, 10
	s_cmp_eq_u32 s33, 15
	v_mov_b32_e32 v207, 0
	v_writelane_b32 v252, s1, 11
	s_cselect_b64 s[0:1], -1, 0
	v_writelane_b32 v252, s0, 42
	s_cmp_eq_u32 s33, 14
	v_mov_b32_e32 v244, 0x8000
	v_writelane_b32 v252, s1, 43
	s_cselect_b64 s[0:1], -1, 0
	v_writelane_b32 v252, s0, 44
	s_cmp_eq_u32 s33, 13
	v_mov_b32_e32 v250, -1
	v_writelane_b32 v252, s1, 45
	s_cselect_b64 s[0:1], -1, 0
	v_writelane_b32 v252, s0, 46
	s_cmp_eq_u32 s33, 12
	v_mov_b32_e32 v245, 1
	v_writelane_b32 v252, s1, 47
	s_cselect_b64 s[0:1], -1, 0
	v_writelane_b32 v252, s0, 48
	s_cmp_eq_u32 s33, 11
	v_mov_b32_e32 v246, 0x358637bd
	v_writelane_b32 v252, s1, 49
	s_cselect_b64 s[0:1], -1, 0
	v_writelane_b32 v252, s0, 50
	s_cmp_eq_u32 s33, 10
	v_mov_b32_e32 v247, 0x800
	v_writelane_b32 v252, s1, 51
	s_cselect_b64 s[0:1], -1, 0
	v_writelane_b32 v252, s0, 52
	s_cmp_eq_u32 s33, 9
	v_mov_b32_e32 v248, 0x1000
	v_writelane_b32 v252, s1, 53
	s_cselect_b64 s[0:1], -1, 0
	v_writelane_b32 v252, s0, 54
	s_cmp_eq_u32 s33, 8
	s_nop 0
	v_writelane_b32 v252, s1, 55
	s_cselect_b64 s[0:1], -1, 0
	v_writelane_b32 v252, s0, 56
	s_cmp_eq_u32 s33, 7
	s_nop 0
	v_writelane_b32 v252, s1, 57
	s_cselect_b64 s[0:1], -1, 0
	v_writelane_b32 v252, s0, 58
	s_cmp_eq_u32 s33, 6
	s_nop 0
	v_writelane_b32 v252, s1, 59
	s_cselect_b64 s[0:1], -1, 0
	v_writelane_b32 v252, s0, 60
	s_cmp_eq_u32 s33, 5
	s_nop 0
	v_writelane_b32 v252, s1, 61
	s_cselect_b64 s[0:1], -1, 0
	v_writelane_b32 v252, s0, 62
	s_cmp_eq_u32 s33, 4
	s_nop 0
	v_writelane_b32 v252, s1, 63
	s_cselect_b64 s[0:1], -1, 0
	v_writelane_b32 v253, s0, 0
	s_cmp_eq_u32 s33, 3
	s_nop 0
	v_writelane_b32 v253, s1, 1
	s_cselect_b64 s[0:1], -1, 0
	v_writelane_b32 v253, s0, 2
	s_cmp_eq_u32 s33, 2
	s_nop 0
	v_writelane_b32 v253, s1, 3
	s_cselect_b64 s[0:1], -1, 0
	v_writelane_b32 v253, s0, 4
	s_cmp_eq_u32 s33, 1
	s_nop 0
	v_writelane_b32 v253, s1, 5
	s_cselect_b64 s[0:1], -1, 0
	v_writelane_b32 v253, s0, 6
	s_cmp_eq_u32 s33, 0
	s_nop 0
	v_writelane_b32 v253, s1, 7
	s_cselect_b64 s[0:1], -1, 0
	v_writelane_b32 v253, s0, 8
	s_nop 1
	v_writelane_b32 v253, s1, 9
	s_lshl_b32 s0, s33, 8
	s_add_u32 s0, s84, s0
	s_addc_u32 s1, s85, 0
	s_add_u32 s2, s0, 0x1400
	s_addc_u32 s3, s1, 0
	v_writelane_b32 v253, s2, 10
	s_add_u32 s0, s0, 0x2400
	s_addc_u32 s1, s1, 0
	v_writelane_b32 v253, s3, 11
	v_writelane_b32 v253, s0, 12
	s_nop 1
	v_writelane_b32 v253, s1, 13
	s_add_u32 s0, s84, 0x3400
	s_addc_u32 s1, s85, 0
	v_writelane_b32 v253, s0, 14
	s_nop 1
	v_writelane_b32 v253, s1, 15
	s_add_u32 s0, s84, 0x3500
	s_addc_u32 s1, s85, 0
	v_writelane_b32 v253, s0, 16
	s_nop 1
	v_writelane_b32 v253, s1, 17
	s_lshl_b32 s0, s94, 1
	v_writelane_b32 v253, s0, 18
	s_add_u32 s0, s84, 0x2f5b8000
	v_writelane_b32 v253, s0, 19
	s_addc_u32 s0, s85, 0
	v_writelane_b32 v253, s0, 20
	s_add_u32 s0, s84, 0x2e88000
	v_writelane_b32 v253, s0, 21
	s_addc_u32 s0, s85, 0
	v_writelane_b32 v253, s0, 22
	s_add_u32 s0, s84, 0x300f8000
	s_addc_u32 s1, s85, 0
	v_writelane_b32 v252, s0, 8
	s_nop 1
	v_writelane_b32 v252, s1, 9
	s_add_u32 s0, s84, 0x3d740000
	s_addc_u32 s1, s85, 0
	s_add_u32 s28, s84, 0x2fc78000
; __global__ void __launch_bounds__(512, 2) fwd(Params p) {
;     ...
;         if (PSEL(2) && IN(pb + 0)) REPLOOP(2) {
;             pg8::EpiStoreBf16 E{(bf16_t*)(ws + WS_PA), INP};
;             if (l == 0) { if (c >= GgA) moe_convert_while(p, lds, pb + 0, GgA);
;                 else { pg8::TileSched S; S.init(ws + WS_H, (bf16_t*)(ws + WS_WTIN), DM, DM, MT / 256, INP / 256, 1, 0, 0, GgA, c, 0); pg8::gemm_phase(lds, pg8::Desc{DM, DM, DM}, S, E); if (nconv) moe_mark_done(p, pb + 0); } }
;             else { pg8::InSchedLast S; S.init(ws + WS_H, (bf16_t*)(ws + WS_WTIN) + (size_t)INP * DM, G, c); pg8::gemm_phase(lds, pg8::Desc{DM, DM, DM}, S, E); }
;             moe_fill(p, lds, pb + 0);
;          REPBAR(2); }
;         SEAM(pb + 0);
;         if (PSEL(3) && IN(pb + 1)) REPLOOP(3) { ph_rowsplit(p, l, lds); __syncthreads();  REPBAR(3); }
;         SEAM(pb + 1);
;         if (PSEL(4) && IN(pb + 2)) REPLOOP(4) {
;     ...
;             if (C_SEL & 1) { pg8::TileSched S; S.init(ws + WS_QA, (bf16_t*)(ws + WS_WTUQ) + (size_t)l * 768 * 384, 384, 384, (l == 0 ? MT : NLAT) / 256, 3, 1, 0, 0, G, c, 0);
;               pg8::EpiQ E{(bf16_t*)(ws + WS_QB), (const f32x2*)(ws + WS_ROPE)}; pg8::gemm_phase(lds, pg8::Desc{384, 384, 384}, S, E); }
;             if (C_SEL & 2) { pg8::TileSched S; S.init(ws + WS_KVA, (bf16_t*)(ws + WS_WTUKV) + (size_t)l * 1024 * 256, 256, 256, MT / 256, 2, 1, 0, 0, G, c, 112);
;               pg8::EpiK E{(bf16_t*)(ws + WS_KC)}; pg8::gemm_phase(lds, pg8::Desc{256, 256, 256}, S, E); }
;             if (C_SEL & 4) { pg8::TileSched S; S.init((bf16_t*)(ws + WS_WTUKV) + (size_t)l * 1024 * 256 + 512 * 256, ws + WS_KVA, 256, 256, 2, MT / 256, 1, 0, 0, G, c, 184);
;               pg8::EpiV E{(bf16_t*)(ws + WS_VT)}; pg8::gemm_phase(lds, pg8::Desc{256, 256, 256}, S, E); }
;             if (C_SEL & 8) { pg8::TileSched S; S.init(ws + WS_UPK, (bf16_t*)(ws + WS_WST) + (size_t)l * 32 * 256 * 256, 512, 256, 3, 1, 32, (size_t)768 * 512 * 2, (size_t)256 * 256 * 2, G, c, G == 256 ? 112 : 0);
;               pg8::EpiS1 E{(float*)(ws + WS_EST)}; pg8::gemm_phase(lds, pg8::Desc{512, 256, 256}, S, E); }
;             if (G == 256) { const int j = c < 112 ? c : (c >= 208 ? 112 + (c - 208) : -1);
;                 if (j >= 0) { unsigned char* wsq = opaque_ptr(p.ws); const int t_ = opaque_tid(); const int nit = (l == 0 ? MT : NLAT) / 8;
	v_writelane_b32 v253, s0, 23
	s_addc_u32 s29, s85, 0
	s_nop 0
	v_writelane_b32 v253, s1, 24
	s_add_u32 s0, s84, 0x2fa8000
	v_writelane_b32 v253, s0, 25
	s_addc_u32 s0, s85, 0
	v_writelane_b32 v253, s0, 26
	s_add_u32 s0, s84, 0x30e78000
	s_addc_u32 s1, s85, 0
	v_writelane_b32 v253, s0, 27
	s_nop 1
	v_writelane_b32 v253, s1, 28
	s_add_u32 s0, s84, 0x31bf8000
	s_addc_u32 s1, s85, 0
	s_add_u32 s30, s84, 0x324f8000
	v_writelane_b32 v253, s0, 29
	s_addc_u32 s31, s85, 0
	s_nop 0
	v_writelane_b32 v253, s1, 30
	s_add_u32 s0, s84, 0x1b5b8000
	v_writelane_b32 v253, s0, 31
	s_addc_u32 s0, s85, 0
	v_writelane_b32 v253, s0, 32
	s_and_b64 s[0:1], s[24:25], exec
	s_cselect_b32 s5, 0x70, 0
	s_add_u32 s0, s84, 0x33cf8000
	s_addc_u32 s1, s85, 0
	v_writelane_b32 v253, s0, 33
	s_nop 1
	v_writelane_b32 v253, s1, 34
	s_add_i32 s0, s92, 0xffffffa0
	s_cmpk_gt_u32 s92, 0xcf
	s_cselect_b32 s0, s0, -1
	s_cmpk_lt_i32 s92, 0x70
	s_cselect_b32 s33, s92, s0
	s_cmp_gt_i32 s33, -1
	s_cselect_b64 s[2:3], -1, 0
	s_cmpk_lt_i32 s92, 0x100
	s_cselect_b64 s[0:1], -1, 0
	v_writelane_b32 v253, s0, 35
	s_nop 1
	v_writelane_b32 v253, s1, 36
	s_add_u32 s0, s84, 0x1bdb8000
	v_writelane_b32 v253, s0, 37
	s_addc_u32 s0, s85, 0
	v_writelane_b32 v253, s0, 38
	s_add_u32 s0, s84, 0x354f8000
	s_addc_u32 s1, s85, 0
	v_writelane_b32 v252, s0, 2
	s_nop 1
	v_writelane_b32 v252, s1, 3
	s_and_b32 s0, s92, 3
	s_lshl_b32 s1, s0, 7
	v_writelane_b32 v253, s1, 39
	v_writelane_b32 v253, s0, 40
	s_lshl_b32 s0, s0, 9
	s_add_u32 s0, s8, s0
	v_writelane_b32 v253, s0, 41
	s_addc_u32 s0, s9, 0
	v_writelane_b32 v253, s0, 42
	s_add_u32 s0, s84, 0xc000
	v_writelane_b32 v253, s0, 43
	s_addc_u32 s0, s85, 0
	v_writelane_b32 v253, s0, 44
	s_add_u32 s0, s84, 0x30a8000
	v_writelane_b32 v253, s0, 45
	s_addc_u32 s0, s85, 0
	v_writelane_b32 v253, s0, 46
	s_add_u32 s0, s84, 0x2d1b8000
	s_addc_u32 s1, s85, 0
	v_writelane_b32 v253, s0, 47
	s_cmpk_lg_i32 s94, 0x100
	s_nop 0
	v_writelane_b32 v253, s1, 48
	s_cselect_b64 s[0:1], -1, 0
	s_add_u32 s8, s84, 0x1e88000
	v_writelane_b32 v253, s8, 49
	s_addc_u32 s8, s85, 0
	v_writelane_b32 v253, s8, 50
	s_add_u32 s8, s84, 0x241b8000
	s_addc_u32 s9, s85, 0
	v_writelane_b32 v253, s8, 51
	s_nop 1
	v_writelane_b32 v253, s9, 52
	s_add_u32 s8, s84, 0x289b8000
	s_addc_u32 s9, s85, 0
	v_writelane_b32 v253, s8, 53
	s_cmp_lt_i32 s92, s4
	s_nop 0
	v_writelane_b32 v253, s9, 54
	s_cselect_b64 s[8:9], -1, 0
	v_writelane_b32 v253, s8, 55
	s_cmp_eq_u32 s4, 0
	s_nop 0
	v_writelane_b32 v253, s9, 56
	v_writelane_b32 v253, s4, 57
	s_cselect_b32 s4, s94, s4
	s_add_u32 s8, s84, 0x4900
	v_writelane_b32 v253, s4, 58
	s_addc_u32 s9, s85, 0
	v_writelane_b32 v253, s8, 59
	s_lshl_b32 s4, s92, 3
	s_nop 0
	v_writelane_b32 v253, s9, 60
	v_writelane_b32 v253, s4, 61
	s_add_u32 s4, s84, 0x31a8000
	v_writelane_b32 v253, s4, 62
	s_addc_u32 s4, s85, 0
	s_add_u32 s8, s84, 0x35f40000
	s_addc_u32 s9, s85, 0
	v_writelane_b32 v254, s8, 0
	s_cmp_lt_i32 s92, s7
	v_writelane_b32 v253, s4, 63
	v_writelane_b32 v254, s9, 1
	s_cselect_b64 s[8:9], -1, 0
	v_writelane_b32 v254, s8, 2
	s_cmp_eq_u32 s7, 0
	s_cselect_b32 s4, s94, s7
	v_writelane_b32 v254, s9, 3
	s_add_u32 s8, s84, 0x35e88000
	v_writelane_b32 v254, s4, 4
	s_addc_u32 s9, s85, 0
	v_writelane_b32 v254, s8, 5
	s_lshl_b32 s4, s92, 1
	s_and_b32 s4, s4, 14
	v_writelane_b32 v254, s9, 6
	v_writelane_b32 v254, s4, 7
	s_ashr_i32 s34, s92, 3
	s_ashr_i32 s4, s92, 31
	s_add_u32 s8, s84, 0x4d00
	v_writelane_b32 v254, s4, 8
	s_addc_u32 s9, s85, 0
	v_writelane_b32 v254, s8, 9
	s_add_u32 s4, s84, 0x131a8000
	s_nop 0
	v_writelane_b32 v254, s9, 10
	v_writelane_b32 v254, s4, 11
	s_addc_u32 s4, s85, 0
	s_add_u32 s8, s84, 0x38740000
	v_writelane_b32 v254, s4, 12
	s_addc_u32 s9, s85, 0
	v_writelane_b32 v254, s8, 13
	s_nop 1
	v_writelane_b32 v254, s9, 14
	s_add_u32 s8, s84, 0x35e9c000
	s_addc_u32 s9, s85, 0
	v_writelane_b32 v254, s8, 15
	s_cmp_ge_i32 s92, s7
	s_nop 0
	v_writelane_b32 v254, s9, 16
	v_writelane_b32 v254, s7, 17
	s_cselect_b64 s[8:9], -1, 0
	v_writelane_b32 v254, s8, 18
	s_nop 1
	v_writelane_b32 v254, s9, 19
	s_add_u32 s8, s84, 0x4e00
	s_addc_u32 s9, s85, 0
	v_writelane_b32 v254, s8, 20
	s_nop 1
	v_writelane_b32 v254, s9, 21
	v_readlane_b32 s8, v251, 0
	v_readlane_b32 s16, v251, 8
	v_readlane_b32 s9, v251, 1
	v_readlane_b32 s11, v251, 3
	v_readlane_b32 s17, v251, 9
	s_add_u32 s8, s16, 0x2000
	s_addc_u32 s9, s17, 0
	s_abs_i32 s11, s94
	v_cvt_f32_u32_e32 v1, s11
	s_sub_i32 s4, 0, s11
	v_readlane_b32 s12, v251, 4
	v_writelane_b32 v254, s8, 22
	v_rcp_iflag_f32_e32 v1, v1
	s_and_b64 s[2:3], s[24:25], s[2:3]
	v_writelane_b32 v254, s9, 23
	v_writelane_b32 v254, s2, 24
	v_mul_f32_e32 v1, 0x4f7ffffe, v1
	v_cvt_u32_f32_e32 v1, v1
	v_writelane_b32 v254, s3, 25
	s_ashr_i32 s2, s27, 31
	v_readlane_b32 s13, v251, 5
	v_readfirstlane_b32 s7, v1
	s_mul_i32 s4, s4, s7
	s_mul_hi_u32 s4, s7, s4
	s_add_i32 s12, s7, s4
	s_abs_i32 s4, s27
	s_mul_hi_u32 s7, s4, s12
	s_mul_i32 s7, s7, s11
	s_sub_i32 s4, s4, s7
	s_sub_i32 s3, s4, s11
	s_cmp_ge_u32 s4, s11
	s_cselect_b32 s3, s3, s4
	s_sub_i32 s4, s3, s11
	s_cmp_ge_u32 s3, s11
	s_cselect_b32 s3, s4, s3
	s_xor_b32 s3, s3, s2
	s_sub_i32 s13, s3, s2
	s_ashr_i32 s2, s13, 31
	s_cmpk_lt_i32 s13, 0x1e0
	v_writelane_b32 v252, s2, 7
	s_cselect_b64 s[2:3], -1, 0
	v_writelane_b32 v254, s2, 26
	s_cmpk_gt_i32 s13, 0x1df
	v_readlane_b32 s14, v251, 6
	v_writelane_b32 v254, s3, 27
	s_cselect_b64 s[2:3], -1, 0
	v_writelane_b32 v254, s2, 28
	s_cmpk_lt_u32 s13, 0x1f0
	s_cselect_b64 s[8:9], -1, 0
	v_writelane_b32 v254, s3, 29
	s_mul_hi_i32 s2, s13, 0x88888889
	s_add_i32 s2, s2, s13
	s_lshr_b32 s3, s2, 31
	s_ashr_i32 s2, s2, 8
	s_add_i32 s2, s2, s3
	s_mulk_i32 s2, 0x1e0
;     __device__ __forceinline__ bool next(int i, Unit& u) const {
;         const int nwg = nM * nN; const long L = (long)i * G + c; if (L >= (long)nwg * nB) return false;
;         const int pb = (int)(L / nwg); int wgid = (int)(L % nwg);
;         { const int q = nwg / 8, r = nwg % 8, xcd = wgid % 8, off = wgid / 8; wgid = (xcd < r ? xcd * (q + 1) : r * (q + 1) + (xcd - r) * q) + off; }
;         const int nig = 8 * nN, gid = wgid / nig, fm = gid * 8, gsz = (nM - fm) < 8 ? (nM - fm) : 8;
;         u.pm = fm + ((wgid % nig) % gsz); u.pn = (wgid % nig) / gsz; u.pb = pb;
;         u.a = A + (size_t)pb * sA + (size_t)u.pm * 256 * lda * 2; u.b = B + (size_t)pb * sB + (size_t)u.pn * 256 * ldb * 2; return true;
;     }
;     __device__ __forceinline__ void init(const void* A_, const void* B_, int G_, int c_) { T.init(A_, B_, DM, DM, NLAT / 256, INP / 256, 1, 0, 0, G_, c_, 0); }
;     __device__ __forceinline__ bool next(int i, Unit& u) const {
;         const int nlat = (NLAT / 256) * (INP / 256); const long L = (long)i * T.G + T.c;
;         if (L < nlat) return T.next(i, u);
;         if (L >= nlat + 16) return false;
;         const int k = (int)(L - nlat); u.pm = NLAT / 256 + (k >> 2); u.pn = 5 + (k & 3); u.pb = 0;
;         u.a = T.A + (size_t)u.pm * 256 * DM * 2; u.b = T.B + (size_t)u.pn * 256 * DM * 2; return true;
	s_sub_i32 s2, s13, s2
	s_sext_i32_i16 s3, s2
	s_bfe_u32 s3, s3, 0x3001c
	s_add_i32 s3, s2, s3
	s_and_b32 s4, s3, 0xfff8
	v_writelane_b32 v254, s8, 30
	s_sub_i32 s2, s2, s4
	s_add_i32 s4, s13, 0xfffffe20
	s_and_b32 s7, s13, 3
	v_writelane_b32 v254, s9, 31
	s_lshr_b32 s4, s4, 2
	s_add_i32 s8, s7, 5
	s_sext_i32_i16 s3, s3
	s_ashr_i32 s3, s3, 3
	s_add_i32 s14, s4, 32
	s_sext_i32_i16 s7, s2
	s_lshl_b32 s4, s8, 20
	s_cmp_lt_i32 s7, 0
	s_cselect_b32 s7, 61, 60
	s_mul_i32 s2, s2, s7
	s_add_i32 s2, s2, s3
	s_sext_i32_i16 s3, s2
	s_mulk_i32 s3, 0x8889
	s_lshr_b32 s3, s3, 16
	s_add_i32 s3, s3, s2
	s_sext_i32_i16 s7, s3
	s_ashr_i32 s7, s7, 6
	s_bfe_u32 s3, s3, 0x1000f
	s_add_i32 s3, s7, s3
	s_mul_i32 s7, s3, 0x78
	s_sub_i32 s2, s2, s7
	s_bfe_i32 s7, s2, 0x80000
	s_bfe_u32 s7, s7, 0x3000c
	s_add_i32 s7, s2, s7
	v_writelane_b32 v254, s8, 32
	s_and_b32 s8, s7, 0xf8
	s_sub_i32 s2, s2, s8
	s_abs_i32 s8, s26
	v_cvt_f32_u32_e32 v1, s8
	s_sext_i32_i16 s3, s3
	s_lshl_b32 s3, s3, 3
	s_sext_i32_i8 s2, s2
	v_rcp_iflag_f32_e32 v1, v1
	v_readlane_b32 s10, v251, 2
	s_add_i32 s2, s3, s2
	v_writelane_b32 v254, s26, 33
	v_mul_f32_e32 v1, 0x4f7ffffe, v1
	v_cvt_u32_f32_e32 v1, v1
	s_sub_i32 s9, 0, s8
	s_bfe_i32 s7, s7, 0x80000
	s_ashr_i32 s3, s2, 31
	v_readfirstlane_b32 s10, v1
	s_mul_i32 s9, s9, s10
	s_sext_i32_i16 s7, s7
	v_writelane_b32 v254, s2, 34
	s_mul_hi_u32 s9, s10, s9
	s_add_i32 s10, s10, s9
	v_writelane_b32 v254, s3, 35
	s_ashr_i32 s2, s7, 3
	s_abs_i32 s9, s6
	v_writelane_b32 v254, s2, 36
	s_lshr_b32 s2, s7, 3
	s_mul_hi_u32 s10, s9, s10
	s_bfe_i64 s[2:3], s[2:3], 0x100000
	s_mul_i32 s10, s10, s8
	s_lshl_b64 s[2:3], s[2:3], 20
	s_sub_i32 s9, s9, s10
	v_writelane_b32 v254, s2, 37
	v_readlane_b32 s15, v251, 7
	v_writelane_b32 v252, s13, 12
	v_writelane_b32 v254, s3, 38
	s_ashr_i32 s2, s6, 31
	s_sub_i32 s3, s9, s8
	s_cmp_ge_u32 s9, s8
	s_cselect_b32 s3, s3, s9
	s_sub_i32 s6, s3, s8
	s_cmp_ge_u32 s3, s8
	s_cselect_b32 s3, s6, s3
	s_xor_b32 s3, s3, s2
	s_sub_i32 s6, s3, s2
	s_ashr_i32 s2, s6, 31
	v_writelane_b32 v254, s2, 39
	s_cmpk_lt_i32 s6, 0x21c
	s_mul_hi_i32 s2, s6, 0xf2b9d649
	s_cselect_b64 s[8:9], -1, 0
	s_add_i32 s2, s2, s6
	s_lshr_b32 s3, s2, 31
	s_ashr_i32 s2, s2, 9
	s_add_i32 s2, s2, s3
	s_mulk_i32 s2, 0x21c
	s_sub_i32 s2, s6, s2
	v_writelane_b32 v254, s8, 40
	s_sext_i32_i16 s3, s2
	s_bfe_u32 s3, s3, 0x3001c
	v_writelane_b32 v254, s9, 41
	v_writelane_b32 v254, s6, 42
	s_add_i32 s6, s2, s3
	s_and_b32 s3, s6, 0xfff8
	s_sub_i32 s3, s2, s3
	s_sext_i32_i16 s2, s6
	s_lshr_b32 s2, s2, 3
	v_writelane_b32 v254, s2, 43
	s_sext_i32_i16 s2, s3
	s_cmp_gt_i32 s2, 3
	s_cselect_b64 s[6:7], -1, 0
	s_mul_i32 s2, s3, 0x43
	v_writelane_b32 v254, s6, 44
	s_add_i32 s2, s2, 4
	v_readlane_b32 s18, v251, 10
	v_writelane_b32 v254, s7, 45
	v_writelane_b32 v254, s2, 46
	s_mul_hi_u32 s2, s12, 0x70
	s_mul_i32 s2, s2, s11
	s_sub_i32 s2, 0x70, s2
	s_abs_i32 s6, s13
	v_writelane_b32 v254, s6, 47
	s_sub_i32 s6, s2, s11
	s_cmp_ge_u32 s2, s11
	s_cselect_b32 s2, s6, s2
	s_sub_i32 s6, s2, s11
	s_cmp_ge_u32 s2, s11
	s_cselect_b32 s2, s6, s2
	s_sub_i32 s2, s27, s2
	s_abs_i32 s6, s2
	s_mul_hi_u32 s7, s6, s12
	s_mul_i32 s7, s7, s11
	s_sub_i32 s6, s6, s7
	s_ashr_i32 s2, s2, 31
	s_sub_i32 s7, s6, s11
	s_cmp_ge_u32 s6, s11
	s_cselect_b32 s6, s7, s6
	s_sub_i32 s7, s6, s11
	s_cmp_ge_u32 s6, s11
	s_cselect_b32 s6, s7, s6
	s_xor_b32 s6, s6, s2
	s_sub_i32 s7, s6, s2
	s_ashr_i32 s2, s7, 31
	v_writelane_b32 v254, s2, 48
	s_cmpk_lt_i32 s7, 0x48
	s_mul_hi_i32 s2, s7, 0x38e38e39
	s_cselect_b64 s[8:9], -1, 0
	s_lshr_b32 s6, s2, 31
	s_ashr_i32 s2, s2, 4
	s_add_i32 s2, s2, s6
	s_mulk_i32 s2, 0x48
	s_sub_i32 s2, s7, s2
	s_bfe_i32 s6, s2, 0x80000
	v_writelane_b32 v254, s8, 49
	s_bfe_u32 s6, s6, 0x3000c
	s_add_i32 s6, s2, s6
	v_writelane_b32 v254, s9, 50
	v_writelane_b32 v254, s7, 51
	s_and_b32 s7, s6, 0xfff8
	s_sub_i32 s2, s2, s7
	s_bfe_i32 s6, s6, 0x80000
	s_sext_i32_i16 s6, s6
	s_bfe_i32 s7, s2, 0x80000
	s_ashr_i32 s6, s6, 3
	s_sext_i32_i16 s7, s7
	s_cmp_lt_i32 s7, 0
	s_cselect_b32 s7, 10, 9
	s_mul_i32 s2, s2, s7
	s_add_i32 s2, s2, s6
	s_bfe_i32 s6, s2, 0x80000
	s_bfe_u32 s6, s6, 0x4000b
	s_add_i32 s6, s2, s6
	s_and_b32 s7, s6, 0xfff0
	s_sub_i32 s8, s2, s7
	s_bfe_i32 s2, s6, 0x80000
	s_sext_i32_i16 s2, s2
	s_ashr_i32 s2, s2, 4
	s_lshl_b32 s9, s2, 3
	s_sub_i32 s2, 36, s9
	s_min_u32 s10, s2, 8
	s_sext_i32_i8 s2, s8
	v_cvt_f32_ubyte0_e32 v2, s10
	v_cvt_f32_i32_e32 v1, s2
	v_rcp_iflag_f32_e32 v3, v2
	s_ashr_i32 s2, s2, 30
	s_or_b32 s2, s2, 1
	v_readlane_b32 s19, v251, 11
	v_mul_f32_e32 v3, v1, v3
	v_trunc_f32_e32 v3, v3
	v_fma_f32 v1, -v3, v2, v1
	v_cmp_ge_f32_e64 s[6:7], |v1|, v2
	v_cvt_i32_f32_e32 v1, v3
	s_and_b64 s[6:7], s[6:7], exec
	s_cselect_b32 s2, s2, 0
	v_readlane_b32 s20, v251, 12
	v_readfirstlane_b32 s6, v1
	s_add_i32 s2, s6, s2
	s_mul_i32 s6, s2, s10
	s_sub_i32 s6, s8, s6
	s_sext_i32_i8 s6, s6
	s_add_i32 s8, s9, s6
	s_mov_b32 s6, s8
	s_ashr_i32 s9, s8, 31
	v_writelane_b32 v254, s6, 52
	v_mbcnt_lo_u32_b32 v1, -1, 0
	v_mbcnt_hi_u32_b32 v249, -1, v1
	v_writelane_b32 v254, s7, 53
	s_lshl_b64 s[6:7], s[8:9], 17
	s_add_u32 s8, s28, s6
	s_addc_u32 s9, s29, s7
	s_bfe_i64 s[6:7], s[2:3], 0x80000
	s_lshl_b64 s[6:7], s[6:7], 17
	v_writelane_b32 v254, s6, 54
	s_sext_i32_i8 s2, s2
	v_mov_b32_e32 v1, 0x500
	v_writelane_b32 v254, s7, 55
	s_add_u32 s6, s8, 0x10000
	v_writelane_b32 v254, s8, 56
	s_addc_u32 s7, s9, 0
	v_readlane_b32 s21, v251, 13
	v_writelane_b32 v254, s9, 57
	v_writelane_b32 v254, s6, 58
	v_readlane_b32 s22, v251, 14
; __device__ __forceinline__ unsigned xb_ld(unsigned* p)              { return __hip_atomic_load(p, __ATOMIC_RELAXED, __HIP_MEMORY_SCOPE_AGENT); }
; __device__ __forceinline__ unsigned xb_add(unsigned* p, unsigned v) { return __hip_atomic_fetch_add(p, v, __ATOMIC_RELAXED, __HIP_MEMORY_SCOPE_AGENT); }
; #define XB_SPIN(cond, bar) do { unsigned _sp = 0; while (cond) { __builtin_amdgcn_s_sleep(1); \
;     if ((++_sp & 255u) == 0u) { if (xb_ld(&(bar)[XB_TMO])) break; if (_sp > XB_SPIN_CAP) { atomicAdd(&(bar)[XB_TMO], 1u); break; } } } } while (0)
; __device__ __forceinline__ void xcd_barrier(const XcdBarrier& b) {
;     ...
;         const unsigned old = xb_add(&bar[XB_XSUB(b.x)], 1u);
;         const unsigned gen = old / nloc;
;         if (old + 1u == (gen + 1u) * nloc) {
;             __builtin_amdgcn_fence(__ATOMIC_RELEASE, "agent");
;             asm volatile("s_waitcnt vmcnt(0)" ::: "memory");
;             const unsigned og = xb_add(&bar[XB_TOP], 1u);
;             const unsigned tg = og / nx;
;             if (og + 1u == (tg + 1u) * nx) xb_add(&bar[XB_TOPGEN], 1u);
;             else XB_SPIN(xb_ld(&bar[XB_TOPGEN]) == tg, bar);
;             __builtin_amdgcn_fence(__ATOMIC_ACQUIRE, "agent");
;             xb_add(&bar[XB_XGEN(b.x)], 1u);
;             asm volatile("s_waitcnt vmcnt(0)" ::: "memory");
;     __device__ __forceinline__ bool next(int i, Unit& u) const {
;         const int nwg = nM * nN; const long L = (long)i * G + c; if (L >= (long)nwg * nB) return false;
;         const int pb = (int)(L / nwg); int wgid = (int)(L % nwg);
;         { const int q = nwg / 8, r = nwg % 8, xcd = wgid % 8, off = wgid / 8; wgid = (xcd < r ? xcd * (q + 1) : r * (q + 1) + (xcd - r) * q) + off; }
;         const int nig = 8 * nN, gid = wgid / nig, fm = gid * 8, gsz = (nM - fm) < 8 ? (nM - fm) : 8;
;         u.pm = fm + ((wgid % nig) % gsz); u.pn = (wgid % nig) / gsz; u.pb = pb;
;         u.a = A + (size_t)pb * sA + (size_t)u.pm * 256 * lda * 2; u.b = B + (size_t)pb * sB + (size_t)u.pn * 256 * ldb * 2; return true;
	v_readlane_b32 s23, v251, 15
	v_writelane_b32 v254, s7, 59
	s_mul_hi_u32 s6, s12, 0xb8
	s_mul_i32 s6, s6, s11
	s_sub_i32 s6, 0xb8, s6
	s_sub_i32 s7, s6, s11
	s_cmp_ge_u32 s6, s11
	s_cselect_b32 s6, s7, s6
	s_sub_i32 s7, s6, s11
	s_cmp_ge_u32 s6, s11
	s_cselect_b32 s6, s7, s6
	s_sub_i32 s6, s27, s6
	s_abs_i32 s7, s6
	s_mul_hi_u32 s8, s7, s12
	s_mul_i32 s8, s8, s11
	s_sub_i32 s7, s7, s8
	s_ashr_i32 s6, s6, 31
	s_sub_i32 s8, s7, s11
	s_cmp_ge_u32 s7, s11
	s_cselect_b32 s7, s8, s7
	s_sub_i32 s8, s7, s11
	s_cmp_ge_u32 s7, s11
	s_cselect_b32 s7, s8, s7
	s_xor_b32 s7, s7, s6
	s_sub_i32 s8, s7, s6
	s_ashr_i32 s6, s8, 31
	v_writelane_b32 v254, s6, 60
	s_cmpk_lt_i32 s8, 0x48
	s_mul_hi_i32 s6, s8, 0x38e38e39
	s_cselect_b64 s[16:17], -1, 0
	s_lshr_b32 s7, s6, 31
	s_ashr_i32 s6, s6, 4
	s_add_i32 s6, s6, s7
	s_mulk_i32 s6, 0x48
	s_sub_i32 s6, s8, s6
	s_bfe_i32 s7, s6, 0x80000
	v_writelane_b32 v254, s16, 61
	s_bfe_u32 s7, s7, 0x3000c
	s_add_i32 s7, s6, s7
	v_writelane_b32 v254, s17, 62
	v_writelane_b32 v254, s8, 63
	s_and_b32 s8, s7, 0xfff8
	s_sub_i32 s6, s6, s8
	s_bfe_i32 s7, s7, 0x80000
	s_sext_i32_i16 s7, s7
	s_bfe_i32 s8, s6, 0x80000
	s_ashr_i32 s7, s7, 3
	s_sext_i32_i16 s8, s8
	s_cmp_lt_i32 s8, 0
	s_cselect_b32 s8, 10, 9
	s_mul_i32 s6, s6, s8
	s_add_i32 s6, s6, s7
	s_bfe_u32 s7, s6, 0x10007
	s_add_i32 s7, s6, s7
	s_bfe_i32 s8, s7, 0x80000
	s_and_b32 s7, s7, 0xfffe
	s_sub_i32 s6, s6, s7
	s_sext_i32_i16 s10, s8
	s_bfe_i64 s[8:9], s[6:7], 0x80000
	s_lshl_b64 s[8:9], s[8:9], 17
	v_writelane_b32 v255, s8, 0
	s_ashr_i32 s7, s10, 1
	s_nop 0
	v_writelane_b32 v255, s9, 1
	s_lshr_b32 s8, s10, 1
	s_bfe_i64 s[8:9], s[8:9], 0x100000
	s_lshl_b64 s[8:9], s[8:9], 17
	s_add_u32 s8, s28, s8
	v_writelane_b32 v255, s7, 2
	s_addc_u32 s9, s29, s9
	v_writelane_b32 v255, s28, 3
	s_add_u32 s16, s8, 0x10000
	v_writelane_b32 v255, s29, 4
	s_addc_u32 s17, s9, 0
	v_writelane_b32 v255, s16, 5
	s_mul_hi_u32 s7, s5, s12
	s_mul_i32 s7, s7, s11
	v_writelane_b32 v255, s17, 6
	s_add_u32 s16, s8, 0x10080
	v_writelane_b32 v255, s8, 7
	s_addc_u32 s17, s9, 0
	s_sub_i32 s5, s5, s7
	s_sub_i32 s7, s5, s11
	s_cmp_ge_u32 s5, s11
	s_cselect_b32 s5, s7, s5
	s_sub_i32 s7, s5, s11
	s_cmp_ge_u32 s5, s11
	s_cselect_b32 s5, s7, s5
	s_sub_i32 s5, s27, s5
	s_abs_i32 s7, s5
	v_writelane_b32 v255, s9, 8
	s_mul_hi_u32 s8, s7, s12
	s_mul_i32 s8, s8, s11
	s_sub_i32 s7, s7, s8
	s_ashr_i32 s5, s5, 31
	s_sub_i32 s8, s7, s11
	s_cmp_ge_u32 s7, s11
	s_cselect_b32 s7, s8, s7
	s_sub_i32 s8, s7, s11
	s_cmp_ge_u32 s7, s11
	s_cselect_b32 s7, s8, s7
	v_writelane_b32 v255, s16, 9
	s_xor_b32 s7, s7, s5
	s_sub_i32 s8, s7, s5
	v_writelane_b32 v255, s17, 10
	v_writelane_b32 v255, s12, 11
	s_ashr_i32 s5, s8, 31
	v_writelane_b32 v255, s11, 12
	s_cmpk_lt_i32 s8, 0x60
	v_writelane_b32 v255, s5, 13
	s_mul_hi_i32 s5, s8, 0x55555556
	s_cselect_b64 s[10:11], -1, 0
	v_writelane_b32 v255, s10, 14
	s_lshr_b32 s7, s5, 31
	s_mov_b64 s[28:29], 0x31bf8100
	v_writelane_b32 v255, s11, 15
	s_add_i32 s10, s5, s7
	s_mul_i32 s5, s10, 3
	s_ashr_i32 s11, s10, 31
	v_writelane_b32 v255, s8, 16
	s_sub_i32 s9, s8, s5
	s_mul_i32 s5, s10, 0xc0000
	v_writelane_b32 v255, s30, 17
	s_add_u32 s5, s30, s5
	s_mul_hi_i32 s7, s10, 0xc0000
	v_writelane_b32 v255, s31, 18
	s_addc_u32 s7, s31, s7
	s_lshl_b32 s8, s9, 24
	s_ashr_i32 s8, s8, 6
	v_writelane_b32 v255, s9, 19
	s_bfe_i32 s9, s9, 0x10007
	s_add_u32 s8, s5, s8
	s_addc_u32 s9, s7, s9
	v_writelane_b32 v255, s8, 20
	s_mov_b32 s5, 0
	s_mov_b32 s15, s5
	v_writelane_b32 v255, s9, 21
	v_writelane_b32 v255, s2, 22
	s_sext_i32_i8 s2, s6
	v_writelane_b32 v255, s2, 23
	v_writelane_b32 v255, s14, 24
	s_mul_i32 s2, s3, 0x44
	s_mov_b64 s[6:7], 0xc000
	v_writelane_b32 v255, s15, 25
	v_writelane_b32 v255, s2, 26
	s_abs_i32 s2, s92
	v_writelane_b32 v255, s2, 27
	v_writelane_b32 v255, s34, 28
	s_abs_i32 s2, s34
	v_writelane_b32 v255, s2, 29
	s_add_i32 s2, s92, 0x480
	v_writelane_b32 v255, s2, 30
	s_mov_b32 s2, s10
	v_writelane_b32 v255, s2, 31
	s_mov_b64 s[8:9], 0x80
	s_nop 0
	v_writelane_b32 v255, s3, 32
	s_lshl_b64 s[2:3], s[10:11], 17
	v_writelane_b32 v255, s2, 33
	s_mov_b64 s[10:11], 0x100
	s_nop 0
	v_writelane_b32 v255, s3, 34
	s_lshl_b32 s2, s33, 3
	v_writelane_b32 v255, s33, 35
	s_add_u32 s3, s84, 0x2d1b8c00
	v_writelane_b32 v255, s3, 36
	s_addc_u32 s3, s85, 0
	v_writelane_b32 v255, s3, 37
	s_ashr_i32 s3, s2, 31
	v_writelane_b32 v255, s2, 38
	s_xor_b64 s[0:1], s[0:1], -1
	s_mov_b32 s33, 0xc0135761
	v_writelane_b32 v255, s3, 39
	v_writelane_b32 v255, s0, 40
	s_nop 1
	v_writelane_b32 v255, s1, 41
	v_writelane_b32 v255, s27, 42
	s_lshl_b32 s0, s27, 3
	v_writelane_b32 v255, s0, 43
	s_lshl_b32 s0, s94, 3
	v_writelane_b32 v255, s0, 44
	s_add_i32 s0, 0, 0x20828
	v_writelane_b32 v255, s0, 45
	s_add_i32 s0, 0, 0x2082c
	v_writelane_b32 v255, s0, 46
	s_add_i32 s0, 0, 0x20820
	v_writelane_b32 v252, s0, 4
	s_add_i32 s0, 0, 0x10400
	v_writelane_b32 v255, s0, 47
	s_add_i32 s0, 0, 0x20824
	v_writelane_b32 v252, s0, 17
	s_add_i32 s0, 0, 0x20800
	v_writelane_b32 v255, s0, 48
	s_add_i32 s0, 0, 0x20804
	v_writelane_b32 v255, s0, 49
	s_add_i32 s0, 0, 0x12c00
	v_writelane_b32 v255, s0, 50
	s_add_i32 s0, 0, 0x17400
	v_writelane_b32 v255, s0, 51
	v_writelane_b32 v255, s4, 52
	s_mov_b64 s[0:1], 0
	s_mov_b32 s2, s5
	v_writelane_b32 v255, s5, 53
	v_writelane_b32 v255, s0, 54
	s_nop 1
	v_writelane_b32 v255, s1, 55
	s_branch .LBB0_206
.LBB0_203:
	s_waitcnt vmcnt(0)
.LBB0_204:
	s_or_b64 exec, exec, s[0:1]
	s_waitcnt lgkmcnt(0)
	s_barrier

; __device__ __forceinline__ unsigned xb_ld(unsigned* p)              { return __hip_atomic_load(p, __ATOMIC_RELAXED, __HIP_MEMORY_SCOPE_AGENT); }
; __device__ __forceinline__ unsigned xb_add(unsigned* p, unsigned v) { return __hip_atomic_fetch_add(p, v, __ATOMIC_RELAXED, __HIP_MEMORY_SCOPE_AGENT); }
; #define XB_SPIN(cond, bar) do { unsigned _sp = 0; while (cond) { __builtin_amdgcn_s_sleep(1); \
;     if ((++_sp & 255u) == 0u) { if (xb_ld(&(bar)[XB_TMO])) break; if (_sp > XB_SPIN_CAP) { atomicAdd(&(bar)[XB_TMO], 1u); break; } } } } while (0)
; __device__ __forceinline__ void xcd_barrier(const XcdBarrier& b) {
;     ...
;     if (threadIdx.x == 0) {
;         unsigned* bar = b.bar;
;         __builtin_amdgcn_s_waitcnt(0);
;         unsigned nloc = b.st[0], nx = b.st[1];
;         if (nloc == 0u) { xcd_barrier_complete(bar, b.x, nloc, nx); b.st[0] = nloc; b.st[1] = nx; }
;         const unsigned old = xb_add(&bar[XB_XSUB(b.x)], 1u);
;         const unsigned gen = old / nloc;
;         if (old + 1u == (gen + 1u) * nloc) {
;             __builtin_amdgcn_fence(__ATOMIC_RELEASE, "agent");
;             asm volatile("s_waitcnt vmcnt(0)" ::: "memory");
;             const unsigned og = xb_add(&bar[XB_TOP], 1u);
;             const unsigned tg = og / nx;
;             if (og + 1u == (tg + 1u) * nx) xb_add(&bar[XB_TOPGEN], 1u);
;             else XB_SPIN(xb_ld(&bar[XB_TOPGEN]) == tg, bar);
;             __builtin_amdgcn_fence(__ATOMIC_ACQUIRE, "agent");
;             xb_add(&bar[XB_XGEN(b.x)], 1u);
;             asm volatile("s_waitcnt vmcnt(0)" ::: "memory");
;         } else {
;             XB_SPIN(xb_ld(&bar[XB_XGEN(b.x)]) == gen, bar);
;             __builtin_amdgcn_fence(__ATOMIC_ACQUIRE, "agent");
;             asm volatile("s_waitcnt vmcnt(0)" ::: "memory");
;         }
.LBB0_413:
	v_readlane_b32 s0, v252, 5
	s_mul_i32 s0, s0, 13
	s_add_i32 s4, s0, 3
	s_cmp_ge_i32 s4, s87
	v_readlane_b32 s1, v252, 6
	s_cbranch_scc1 .LBB0_463
	s_waitcnt vmcnt(0)
	s_waitcnt vmcnt(0)
	s_barrier
	s_mov_b64 s[0:1], exec
	v_readlane_b32 s2, v252, 34
	v_readlane_b32 s3, v252, 35
	s_and_b64 s[2:3], s[0:1], s[2:3]
	s_mov_b64 exec, s[2:3]
	s_cbranch_execz .LBB0_462
	v_readlane_b32 s12, v253, 10
	v_readlane_b32 s13, v253, 11
	v_readlane_b32 s14, v253, 14
	v_readlane_b32 s15, v253, 15
	v_mov_b32_e32 v2, 0x20800
	ds_read_b96 v[4:6], v2
	s_nop 3
	global_atomic_add v3, v207, v245, s[12:13] sc0
	buffer_inv sc1
	s_waitcnt vmcnt(1) lgkmcnt(0)
	v_readfirstlane_b32 s16, v4
	v_readfirstlane_b32 s17, v5
	v_readfirstlane_b32 s24, v6
	v_readfirstlane_b32 s25, v3
	s_add_u32 s24, s24, 1
	v_mov_b32_e32 v6, s24
	ds_write_b32 v2, v6 offset:8
	s_mul_i32 s16, s16, s24
	s_mul_i32 s17, s17, s24
	s_add_u32 s25, s25, 1
	s_cmp_lg_u32 s25, s16
	s_cbranch_scc1 .Lxb3_poll0
	buffer_wbl2 sc1
	s_waitcnt vmcnt(0)
	global_atomic_add v207, v245, s[14:15]
.Lxb3_poll0:
	s_mov_b32 s16, 0
.Lxb3_poll:
	global_load_dword v3, v207, s[14:15] sc1
	s_waitcnt vmcnt(0)
	v_readfirstlane_b32 s25, v3
	s_cmp_ge_u32 s25, s17
	s_cbranch_scc1 .Lxb3_done
	s_sleep 1
	s_add_u32 s16, s16, 1
	s_cmp_lt_u32 s16, 0x400000
	s_cbranch_scc1 .Lxb3_poll

; __device__ __forceinline__ unsigned xb_ld(unsigned* p)              { return __hip_atomic_load(p, __ATOMIC_RELAXED, __HIP_MEMORY_SCOPE_AGENT); }
; __device__ __forceinline__ unsigned xb_add(unsigned* p, unsigned v) { return __hip_atomic_fetch_add(p, v, __ATOMIC_RELAXED, __HIP_MEMORY_SCOPE_AGENT); }
; #define XB_SPIN(cond, bar) do { unsigned _sp = 0; while (cond) { __builtin_amdgcn_s_sleep(1); \
;     if ((++_sp & 255u) == 0u) { if (xb_ld(&(bar)[XB_TMO])) break; if (_sp > XB_SPIN_CAP) { atomicAdd(&(bar)[XB_TMO], 1u); break; } } } } while (0)
; __device__ __forceinline__ void xcd_barrier(const XcdBarrier& b) {
;     ...
;     if (threadIdx.x == 0) {
;         unsigned* bar = b.bar;
;         __builtin_amdgcn_s_waitcnt(0);
;         unsigned nloc = b.st[0], nx = b.st[1];
;         if (nloc == 0u) { xcd_barrier_complete(bar, b.x, nloc, nx); b.st[0] = nloc; b.st[1] = nx; }
;         const unsigned old = xb_add(&bar[XB_XSUB(b.x)], 1u);
;         const unsigned gen = old / nloc;
;         if (old + 1u == (gen + 1u) * nloc) {
;             __builtin_amdgcn_fence(__ATOMIC_RELEASE, "agent");
;             asm volatile("s_waitcnt vmcnt(0)" ::: "memory");
;             const unsigned og = xb_add(&bar[XB_TOP], 1u);
;             const unsigned tg = og / nx;
;             if (og + 1u == (tg + 1u) * nx) xb_add(&bar[XB_TOPGEN], 1u);
;             else XB_SPIN(xb_ld(&bar[XB_TOPGEN]) == tg, bar);
;             __builtin_amdgcn_fence(__ATOMIC_ACQUIRE, "agent");
;             xb_add(&bar[XB_XGEN(b.x)], 1u);
;             asm volatile("s_waitcnt vmcnt(0)" ::: "memory");
;         } else {
;             XB_SPIN(xb_ld(&bar[XB_XGEN(b.x)]) == gen, bar);
;             __builtin_amdgcn_fence(__ATOMIC_ACQUIRE, "agent");
;             asm volatile("s_waitcnt vmcnt(0)" ::: "memory");
;         }
.LBB0_539:
	s_and_b64 vcc, exec, s[0:1]
	s_mov_b32 s27, s31
	s_mov_b32 s31, s30
	s_cbranch_vccz .LBB0_469
	v_readlane_b32 s0, v255, 56
	s_add_i32 s4, s0, 4
	s_cmp_ge_i32 s4, s87
	s_barrier
	s_cbranch_scc1 .LBB0_590
	s_waitcnt vmcnt(0)
	s_barrier
	s_mov_b64 s[0:1], exec
	v_readlane_b32 s2, v252, 34
	v_readlane_b32 s3, v252, 35
	s_and_b64 s[2:3], s[0:1], s[2:3]
	s_mov_b64 exec, s[2:3]
	s_cbranch_execz .LBB0_589
	v_readlane_b32 s12, v253, 10
	v_readlane_b32 s13, v253, 11
	v_readlane_b32 s14, v253, 14
	v_readlane_b32 s15, v253, 15
	v_mov_b32_e32 v2, 0x20800
	ds_read_b96 v[4:6], v2
	s_nop 3
	global_atomic_add v3, v207, v245, s[12:13] sc0
	buffer_inv sc1
	s_waitcnt vmcnt(1) lgkmcnt(0)
	v_readfirstlane_b32 s16, v4
	v_readfirstlane_b32 s17, v5
	v_readfirstlane_b32 s24, v6
	v_readfirstlane_b32 s25, v3
	s_add_u32 s24, s24, 1
	v_mov_b32_e32 v6, s24
	ds_write_b32 v2, v6 offset:8
	s_mul_i32 s16, s16, s24
	s_mul_i32 s17, s17, s24
	s_add_u32 s25, s25, 1
	s_cmp_lg_u32 s25, s16
	s_cbranch_scc1 .Lxb4_poll0
	buffer_wbl2 sc1
	s_waitcnt vmcnt(0)
	global_atomic_add v207, v245, s[14:15]

; __device__ __forceinline__ unsigned xb_ld(unsigned* p)              { return __hip_atomic_load(p, __ATOMIC_RELAXED, __HIP_MEMORY_SCOPE_AGENT); }
; __device__ __forceinline__ unsigned xb_add(unsigned* p, unsigned v) { return __hip_atomic_fetch_add(p, v, __ATOMIC_RELAXED, __HIP_MEMORY_SCOPE_AGENT); }
; #define XB_SPIN(cond, bar) do { unsigned _sp = 0; while (cond) { __builtin_amdgcn_s_sleep(1); \
;     if ((++_sp & 255u) == 0u) { if (xb_ld(&(bar)[XB_TMO])) break; if (_sp > XB_SPIN_CAP) { atomicAdd(&(bar)[XB_TMO], 1u); break; } } } } while (0)
; __device__ __forceinline__ void xcd_barrier(const XcdBarrier& b) {
;     ...
;     if (threadIdx.x == 0) {
;         unsigned* bar = b.bar;
;         __builtin_amdgcn_s_waitcnt(0);
;         unsigned nloc = b.st[0], nx = b.st[1];
;         if (nloc == 0u) { xcd_barrier_complete(bar, b.x, nloc, nx); b.st[0] = nloc; b.st[1] = nx; }
;         const unsigned old = xb_add(&bar[XB_XSUB(b.x)], 1u);
;         const unsigned gen = old / nloc;
;         if (old + 1u == (gen + 1u) * nloc) {
;             __builtin_amdgcn_fence(__ATOMIC_RELEASE, "agent");
;             asm volatile("s_waitcnt vmcnt(0)" ::: "memory");
;             const unsigned og = xb_add(&bar[XB_TOP], 1u);
;             const unsigned tg = og / nx;
;             if (og + 1u == (tg + 1u) * nx) xb_add(&bar[XB_TOPGEN], 1u);
;             else XB_SPIN(xb_ld(&bar[XB_TOPGEN]) == tg, bar);
;             __builtin_amdgcn_fence(__ATOMIC_ACQUIRE, "agent");
;             xb_add(&bar[XB_XGEN(b.x)], 1u);
;             asm volatile("s_waitcnt vmcnt(0)" ::: "memory");
;         } else {
;             XB_SPIN(xb_ld(&bar[XB_XGEN(b.x)]) == gen, bar);
;             __builtin_amdgcn_fence(__ATOMIC_ACQUIRE, "agent");
;             asm volatile("s_waitcnt vmcnt(0)" ::: "memory");
;         }
.LBB0_733:
	v_readlane_b32 s0, v255, 56
	s_add_i32 s4, s0, 5
	s_cmp_ge_i32 s4, s87
	s_cbranch_scc1 .LBB0_783
	s_waitcnt vmcnt(0)
	s_waitcnt vmcnt(0)
	s_barrier
	s_mov_b64 s[0:1], exec
	v_readlane_b32 s2, v252, 34
	v_readlane_b32 s3, v252, 35
	s_and_b64 s[2:3], s[0:1], s[2:3]
	s_mov_b64 exec, s[2:3]
	s_cbranch_execz .LBB0_782
	v_readlane_b32 s12, v253, 10
	v_readlane_b32 s13, v253, 11
	v_readlane_b32 s14, v253, 14
	v_readlane_b32 s15, v253, 15
	v_mov_b32_e32 v2, 0x20800
	ds_read_b96 v[4:6], v2
	s_nop 3
	global_atomic_add v3, v207, v245, s[12:13] sc0
	buffer_inv sc1
	s_waitcnt vmcnt(1) lgkmcnt(0)
	v_readfirstlane_b32 s16, v4
	v_readfirstlane_b32 s17, v5
	v_readfirstlane_b32 s24, v6
	v_readfirstlane_b32 s25, v3
	s_add_u32 s24, s24, 1
	v_mov_b32_e32 v6, s24
	ds_write_b32 v2, v6 offset:8
	s_mul_i32 s16, s16, s24
	s_mul_i32 s17, s17, s24
	s_add_u32 s25, s25, 1
	s_cmp_lg_u32 s25, s16
	s_cbranch_scc1 .Lxb5_poll0
	buffer_wbl2 sc1
	s_waitcnt vmcnt(0)
	global_atomic_add v207, v245, s[14:15]

; __device__ __forceinline__ unsigned xb_ld(unsigned* p)              { return __hip_atomic_load(p, __ATOMIC_RELAXED, __HIP_MEMORY_SCOPE_AGENT); }
; __device__ __forceinline__ unsigned xb_add(unsigned* p, unsigned v) { return __hip_atomic_fetch_add(p, v, __ATOMIC_RELAXED, __HIP_MEMORY_SCOPE_AGENT); }
; #define XB_SPIN(cond, bar) do { unsigned _sp = 0; while (cond) { __builtin_amdgcn_s_sleep(1); \
;     if ((++_sp & 255u) == 0u) { if (xb_ld(&(bar)[XB_TMO])) break; if (_sp > XB_SPIN_CAP) { atomicAdd(&(bar)[XB_TMO], 1u); break; } } } } while (0)
; __device__ __forceinline__ void xcd_barrier(const XcdBarrier& b) {
;     ...
;     if (threadIdx.x == 0) {
;         unsigned* bar = b.bar;
;         __builtin_amdgcn_s_waitcnt(0);
;         unsigned nloc = b.st[0], nx = b.st[1];
;         if (nloc == 0u) { xcd_barrier_complete(bar, b.x, nloc, nx); b.st[0] = nloc; b.st[1] = nx; }
;         const unsigned old = xb_add(&bar[XB_XSUB(b.x)], 1u);
;         const unsigned gen = old / nloc;
;         if (old + 1u == (gen + 1u) * nloc) {
;             __builtin_amdgcn_fence(__ATOMIC_RELEASE, "agent");
;             asm volatile("s_waitcnt vmcnt(0)" ::: "memory");
;             const unsigned og = xb_add(&bar[XB_TOP], 1u);
;             const unsigned tg = og / nx;
;             if (og + 1u == (tg + 1u) * nx) xb_add(&bar[XB_TOPGEN], 1u);
;             else XB_SPIN(xb_ld(&bar[XB_TOPGEN]) == tg, bar);
;             __builtin_amdgcn_fence(__ATOMIC_ACQUIRE, "agent");
;             xb_add(&bar[XB_XGEN(b.x)], 1u);
;             asm volatile("s_waitcnt vmcnt(0)" ::: "memory");
;         } else {
;             XB_SPIN(xb_ld(&bar[XB_XGEN(b.x)]) == gen, bar);
;             __builtin_amdgcn_fence(__ATOMIC_ACQUIRE, "agent");
;             asm volatile("s_waitcnt vmcnt(0)" ::: "memory");
;         }
.LBB0_1341:
	v_readlane_b32 s1, v255, 56
	s_add_i32 s0, s1, 6
	s_cmp_le_i32 s86, s0
	s_cselect_b64 s[2:3], -1, 0
	s_cmp_lt_i32 s0, s87
	s_cselect_b64 s[12:13], -1, 0
	s_add_i32 s4, s1, 7
	s_cmp_lt_i32 s4, s87
	s_cselect_b64 s[0:1], -1, 0
	s_and_b64 s[12:13], s[12:13], s[0:1]
	s_and_b64 s[2:3], s[12:13], s[2:3]
	s_andn2_b64 vcc, exec, s[2:3]
	s_cbranch_vccnz .LBB0_1391
	s_waitcnt vmcnt(0)
	s_waitcnt vmcnt(0)
	s_barrier
	s_mov_b64 s[2:3], exec
	v_readlane_b32 s12, v252, 34
	v_readlane_b32 s13, v252, 35
	s_and_b64 s[12:13], s[2:3], s[12:13]
	s_mov_b64 exec, s[12:13]
	s_cbranch_execz .LBB0_1390
	v_readlane_b32 s12, v253, 10
	v_readlane_b32 s13, v253, 11
	v_readlane_b32 s14, v253, 14
	v_readlane_b32 s15, v253, 15
	v_mov_b32_e32 v2, 0x20800
	ds_read_b96 v[4:6], v2
	s_nop 3
	global_atomic_add v3, v207, v245, s[12:13] sc0
	buffer_inv sc1
	s_waitcnt vmcnt(1) lgkmcnt(0)
	v_readfirstlane_b32 s16, v4
	v_readfirstlane_b32 s17, v5
	v_readfirstlane_b32 s24, v6
	v_readfirstlane_b32 s25, v3
	s_add_u32 s24, s24, 1
	v_mov_b32_e32 v6, s24
	ds_write_b32 v2, v6 offset:8
	s_mul_i32 s16, s16, s24
	s_mul_i32 s17, s17, s24
	s_add_u32 s25, s25, 1
	s_cmp_lg_u32 s25, s16
	s_cbranch_scc1 .Lxb6_poll0
	buffer_wbl2 sc1
	s_waitcnt vmcnt(0)
	global_atomic_add v207, v245, s[14:15]

; __device__ __forceinline__ unsigned xb_ld(unsigned* p)              { return __hip_atomic_load(p, __ATOMIC_RELAXED, __HIP_MEMORY_SCOPE_AGENT); }
; __device__ __forceinline__ unsigned xb_add(unsigned* p, unsigned v) { return __hip_atomic_fetch_add(p, v, __ATOMIC_RELAXED, __HIP_MEMORY_SCOPE_AGENT); }
; #define XB_SPIN(cond, bar) do { unsigned _sp = 0; while (cond) { __builtin_amdgcn_s_sleep(1); \
;     if ((++_sp & 255u) == 0u) { if (xb_ld(&(bar)[XB_TMO])) break; if (_sp > XB_SPIN_CAP) { atomicAdd(&(bar)[XB_TMO], 1u); break; } } } } while (0)
; __device__ __forceinline__ void xcd_barrier(const XcdBarrier& b) {
;     ...
;     if (threadIdx.x == 0) {
;         unsigned* bar = b.bar;
;         __builtin_amdgcn_s_waitcnt(0);
;         unsigned nloc = b.st[0], nx = b.st[1];
;         if (nloc == 0u) { xcd_barrier_complete(bar, b.x, nloc, nx); b.st[0] = nloc; b.st[1] = nx; }
;         const unsigned old = xb_add(&bar[XB_XSUB(b.x)], 1u);
;         const unsigned gen = old / nloc;
;         if (old + 1u == (gen + 1u) * nloc) {
;             __builtin_amdgcn_fence(__ATOMIC_RELEASE, "agent");
;             asm volatile("s_waitcnt vmcnt(0)" ::: "memory");
;             const unsigned og = xb_add(&bar[XB_TOP], 1u);
;             const unsigned tg = og / nx;
;             if (og + 1u == (tg + 1u) * nx) xb_add(&bar[XB_TOPGEN], 1u);
;             else XB_SPIN(xb_ld(&bar[XB_TOPGEN]) == tg, bar);
;             __builtin_amdgcn_fence(__ATOMIC_ACQUIRE, "agent");
;             xb_add(&bar[XB_XGEN(b.x)], 1u);
;             asm volatile("s_waitcnt vmcnt(0)" ::: "memory");
;         } else {
;             XB_SPIN(xb_ld(&bar[XB_XGEN(b.x)]) == gen, bar);
;             __builtin_amdgcn_fence(__ATOMIC_ACQUIRE, "agent");
;             asm volatile("s_waitcnt vmcnt(0)" ::: "memory");
;         }
.LBB0_1451:
	v_readlane_b32 s0, v255, 56
	s_add_i32 s4, s0, 8
	s_cmp_ge_i32 s4, s87
	s_cbranch_scc1 .LBB0_1501
	s_waitcnt vmcnt(0)
	s_waitcnt vmcnt(0)
	s_barrier
	s_mov_b64 s[0:1], exec
	v_readlane_b32 s2, v252, 34
	v_readlane_b32 s3, v252, 35
	s_and_b64 s[2:3], s[0:1], s[2:3]
	s_mov_b64 exec, s[2:3]
	s_cbranch_execz .LBB0_1500
	v_readlane_b32 s12, v253, 10
	v_readlane_b32 s13, v253, 11
	v_readlane_b32 s14, v253, 14
	v_readlane_b32 s15, v253, 15
	v_mov_b32_e32 v2, 0x20800
	ds_read_b96 v[4:6], v2
	s_nop 3
	global_atomic_add v3, v207, v245, s[12:13] sc0
	buffer_inv sc1
	s_waitcnt vmcnt(1) lgkmcnt(0)
	v_readfirstlane_b32 s16, v4
	v_readfirstlane_b32 s17, v5
	v_readfirstlane_b32 s24, v6
	v_readfirstlane_b32 s25, v3
	s_add_u32 s24, s24, 1
	v_mov_b32_e32 v6, s24
	ds_write_b32 v2, v6 offset:8
	s_mul_i32 s16, s16, s24
	s_mul_i32 s17, s17, s24
	s_add_u32 s25, s25, 1
	s_cmp_lg_u32 s25, s16
	s_cbranch_scc1 .Lxb7_poll0
	buffer_wbl2 sc1
	s_waitcnt vmcnt(0)
	global_atomic_add v207, v245, s[14:15]

; __device__ __forceinline__ unsigned xb_ld(unsigned* p)              { return __hip_atomic_load(p, __ATOMIC_RELAXED, __HIP_MEMORY_SCOPE_AGENT); }
; __device__ __forceinline__ unsigned xb_add(unsigned* p, unsigned v) { return __hip_atomic_fetch_add(p, v, __ATOMIC_RELAXED, __HIP_MEMORY_SCOPE_AGENT); }
; #define XB_SPIN(cond, bar) do { unsigned _sp = 0; while (cond) { __builtin_amdgcn_s_sleep(1); \
;     if ((++_sp & 255u) == 0u) { if (xb_ld(&(bar)[XB_TMO])) break; if (_sp > XB_SPIN_CAP) { atomicAdd(&(bar)[XB_TMO], 1u); break; } } } } while (0)
; __device__ __forceinline__ void xcd_barrier(const XcdBarrier& b) {
;     ...
;     if (threadIdx.x == 0) {
;         unsigned* bar = b.bar;
;         __builtin_amdgcn_s_waitcnt(0);
;         unsigned nloc = b.st[0], nx = b.st[1];
;         if (nloc == 0u) { xcd_barrier_complete(bar, b.x, nloc, nx); b.st[0] = nloc; b.st[1] = nx; }
;         const unsigned old = xb_add(&bar[XB_XSUB(b.x)], 1u);
;         const unsigned gen = old / nloc;
;         if (old + 1u == (gen + 1u) * nloc) {
;             __builtin_amdgcn_fence(__ATOMIC_RELEASE, "agent");
;             asm volatile("s_waitcnt vmcnt(0)" ::: "memory");
;             const unsigned og = xb_add(&bar[XB_TOP], 1u);
;             const unsigned tg = og / nx;
;             if (og + 1u == (tg + 1u) * nx) xb_add(&bar[XB_TOPGEN], 1u);
;             else XB_SPIN(xb_ld(&bar[XB_TOPGEN]) == tg, bar);
;             __builtin_amdgcn_fence(__ATOMIC_ACQUIRE, "agent");
;             xb_add(&bar[XB_XGEN(b.x)], 1u);
;             asm volatile("s_waitcnt vmcnt(0)" ::: "memory");
;         } else {
;             XB_SPIN(xb_ld(&bar[XB_XGEN(b.x)]) == gen, bar);
;             __builtin_amdgcn_fence(__ATOMIC_ACQUIRE, "agent");
;             asm volatile("s_waitcnt vmcnt(0)" ::: "memory");
;         }
.LBB0_1702:
	v_readlane_b32 s0, v255, 56
	s_add_i32 s4, s0, 9
	s_cmp_ge_i32 s4, s87
	s_cbranch_scc1 .LBB0_1752
	s_waitcnt vmcnt(0)
	s_waitcnt vmcnt(0)
	s_barrier
	s_mov_b64 s[0:1], exec
	v_readlane_b32 s2, v252, 34
	v_readlane_b32 s3, v252, 35
	s_and_b64 s[2:3], s[0:1], s[2:3]
	s_mov_b64 exec, s[2:3]
	s_cbranch_execz .LBB0_1751
	v_readlane_b32 s12, v253, 10
	v_readlane_b32 s13, v253, 11
	v_readlane_b32 s14, v253, 14
	v_readlane_b32 s15, v253, 15
	v_mov_b32_e32 v2, 0x20800
	ds_read_b96 v[4:6], v2
	s_nop 3
	global_atomic_add v3, v207, v245, s[12:13] sc0
	buffer_inv sc1
	s_waitcnt vmcnt(1) lgkmcnt(0)
	v_readfirstlane_b32 s16, v4
	v_readfirstlane_b32 s17, v5
	v_readfirstlane_b32 s24, v6
	v_readfirstlane_b32 s25, v3
	s_add_u32 s24, s24, 1
	v_mov_b32_e32 v6, s24
	ds_write_b32 v2, v6 offset:8
	s_mul_i32 s16, s16, s24
	s_mul_i32 s17, s17, s24
	s_add_u32 s25, s25, 1
	s_cmp_lg_u32 s25, s16
	s_cbranch_scc1 .Lxb8_poll0
	buffer_wbl2 sc1
	s_waitcnt vmcnt(0)
	global_atomic_add v207, v245, s[14:15]

; __device__ __forceinline__ unsigned xb_ld(unsigned* p)              { return __hip_atomic_load(p, __ATOMIC_RELAXED, __HIP_MEMORY_SCOPE_AGENT); }
; __device__ __forceinline__ unsigned xb_add(unsigned* p, unsigned v) { return __hip_atomic_fetch_add(p, v, __ATOMIC_RELAXED, __HIP_MEMORY_SCOPE_AGENT); }
; #define XB_SPIN(cond, bar) do { unsigned _sp = 0; while (cond) { __builtin_amdgcn_s_sleep(1); \
;     if ((++_sp & 255u) == 0u) { if (xb_ld(&(bar)[XB_TMO])) break; if (_sp > XB_SPIN_CAP) { atomicAdd(&(bar)[XB_TMO], 1u); break; } } } } while (0)
; __device__ __forceinline__ void xcd_barrier(const XcdBarrier& b) {
;     ...
;     if (threadIdx.x == 0) {
;         unsigned* bar = b.bar;
;         __builtin_amdgcn_s_waitcnt(0);
;         unsigned nloc = b.st[0], nx = b.st[1];
;         if (nloc == 0u) { xcd_barrier_complete(bar, b.x, nloc, nx); b.st[0] = nloc; b.st[1] = nx; }
;         const unsigned old = xb_add(&bar[XB_XSUB(b.x)], 1u);
;         const unsigned gen = old / nloc;
;         if (old + 1u == (gen + 1u) * nloc) {
;             __builtin_amdgcn_fence(__ATOMIC_RELEASE, "agent");
;             asm volatile("s_waitcnt vmcnt(0)" ::: "memory");
;             const unsigned og = xb_add(&bar[XB_TOP], 1u);
;             const unsigned tg = og / nx;
;             if (og + 1u == (tg + 1u) * nx) xb_add(&bar[XB_TOPGEN], 1u);
;             else XB_SPIN(xb_ld(&bar[XB_TOPGEN]) == tg, bar);
;             __builtin_amdgcn_fence(__ATOMIC_ACQUIRE, "agent");
;             xb_add(&bar[XB_XGEN(b.x)], 1u);
;             asm volatile("s_waitcnt vmcnt(0)" ::: "memory");
;         } else {
;             XB_SPIN(xb_ld(&bar[XB_XGEN(b.x)]) == gen, bar);
;             __builtin_amdgcn_fence(__ATOMIC_ACQUIRE, "agent");
;             asm volatile("s_waitcnt vmcnt(0)" ::: "memory");
;         }
.LBB0_1762:
	v_readlane_b32 s0, v255, 56
	s_add_i32 s4, s0, 10
	s_cmp_ge_i32 s4, s87
	s_waitcnt lgkmcnt(0)
	s_barrier
	s_cbranch_scc1 .LBB0_1812
	s_waitcnt vmcnt(0)
	s_barrier
	s_mov_b64 s[0:1], exec
	v_readlane_b32 s2, v252, 34
	v_readlane_b32 s3, v252, 35
	s_and_b64 s[2:3], s[0:1], s[2:3]
	s_mov_b64 exec, s[2:3]
	s_cbranch_execz .LBB0_1811
	v_readlane_b32 s12, v253, 10
	v_readlane_b32 s13, v253, 11
	v_readlane_b32 s14, v253, 14
	v_readlane_b32 s15, v253, 15
	v_mov_b32_e32 v2, 0x20800
	ds_read_b96 v[4:6], v2
	s_nop 3
	global_atomic_add v3, v207, v245, s[12:13] sc0
	buffer_inv sc1
	s_waitcnt vmcnt(1) lgkmcnt(0)
	v_readfirstlane_b32 s16, v4
	v_readfirstlane_b32 s17, v5
	v_readfirstlane_b32 s24, v6
	v_readfirstlane_b32 s25, v3
	s_add_u32 s24, s24, 1
	v_mov_b32_e32 v6, s24
	ds_write_b32 v2, v6 offset:8
	s_mul_i32 s16, s16, s24
	s_mul_i32 s17, s17, s24
	s_add_u32 s25, s25, 1
	s_cmp_lg_u32 s25, s16
	s_cbranch_scc1 .Lxb9_poll0
	buffer_wbl2 sc1
	s_waitcnt vmcnt(0)
	global_atomic_add v207, v245, s[14:15]

; __device__ __forceinline__ unsigned xb_ld(unsigned* p)              { return __hip_atomic_load(p, __ATOMIC_RELAXED, __HIP_MEMORY_SCOPE_AGENT); }
; __device__ __forceinline__ unsigned xb_add(unsigned* p, unsigned v) { return __hip_atomic_fetch_add(p, v, __ATOMIC_RELAXED, __HIP_MEMORY_SCOPE_AGENT); }
; #define XB_SPIN(cond, bar) do { unsigned _sp = 0; while (cond) { __builtin_amdgcn_s_sleep(1); \
;     if ((++_sp & 255u) == 0u) { if (xb_ld(&(bar)[XB_TMO])) break; if (_sp > XB_SPIN_CAP) { atomicAdd(&(bar)[XB_TMO], 1u); break; } } } } while (0)
; __device__ __forceinline__ void xcd_barrier(const XcdBarrier& b) {
;     ...
;     if (threadIdx.x == 0) {
;         unsigned* bar = b.bar;
;         __builtin_amdgcn_s_waitcnt(0);
;         unsigned nloc = b.st[0], nx = b.st[1];
;         if (nloc == 0u) { xcd_barrier_complete(bar, b.x, nloc, nx); b.st[0] = nloc; b.st[1] = nx; }
;         const unsigned old = xb_add(&bar[XB_XSUB(b.x)], 1u);
;         const unsigned gen = old / nloc;
;         if (old + 1u == (gen + 1u) * nloc) {
;             __builtin_amdgcn_fence(__ATOMIC_RELEASE, "agent");
;             asm volatile("s_waitcnt vmcnt(0)" ::: "memory");
;             const unsigned og = xb_add(&bar[XB_TOP], 1u);
;             const unsigned tg = og / nx;
;             if (og + 1u == (tg + 1u) * nx) xb_add(&bar[XB_TOPGEN], 1u);
;             else XB_SPIN(xb_ld(&bar[XB_TOPGEN]) == tg, bar);
;             __builtin_amdgcn_fence(__ATOMIC_ACQUIRE, "agent");
;             xb_add(&bar[XB_XGEN(b.x)], 1u);
;             asm volatile("s_waitcnt vmcnt(0)" ::: "memory");
;         } else {
;             XB_SPIN(xb_ld(&bar[XB_XGEN(b.x)]) == gen, bar);
;             __builtin_amdgcn_fence(__ATOMIC_ACQUIRE, "agent");
;             asm volatile("s_waitcnt vmcnt(0)" ::: "memory");
;         }
.LBB0_2011:
	v_readlane_b32 s1, v255, 56
	s_add_i32 s0, s1, 11
	s_cmp_le_i32 s86, s0
	s_cselect_b64 s[2:3], -1, 0
	s_cmp_lt_i32 s0, s87
	s_cselect_b64 s[12:13], -1, 0
	s_add_i32 s4, s1, 12
	s_cmp_lt_i32 s4, s87
	s_cselect_b64 s[0:1], -1, 0
	s_and_b64 s[12:13], s[12:13], s[0:1]
	s_and_b64 s[2:3], s[12:13], s[2:3]
	s_andn2_b64 vcc, exec, s[2:3]
	s_cbranch_vccnz .LBB0_2061
	s_waitcnt vmcnt(0)
	s_waitcnt vmcnt(0)
	s_barrier
	s_mov_b64 s[2:3], exec
	v_readlane_b32 s12, v252, 34
	v_readlane_b32 s13, v252, 35
	s_and_b64 s[12:13], s[2:3], s[12:13]
	s_mov_b64 exec, s[12:13]
	s_cbranch_execz .LBB0_2060
	v_readlane_b32 s12, v253, 10
	v_readlane_b32 s13, v253, 11
	v_readlane_b32 s14, v253, 14
	v_readlane_b32 s15, v253, 15
	v_mov_b32_e32 v2, 0x20800
	ds_read_b96 v[4:6], v2
	s_nop 3
	global_atomic_add v3, v207, v245, s[12:13] sc0
	buffer_inv sc1
	s_waitcnt vmcnt(1) lgkmcnt(0)
	v_readfirstlane_b32 s16, v4
	v_readfirstlane_b32 s17, v5
	v_readfirstlane_b32 s24, v6
	v_readfirstlane_b32 s25, v3
	s_add_u32 s24, s24, 1
	v_mov_b32_e32 v6, s24
	ds_write_b32 v2, v6 offset:8
	s_mul_i32 s16, s16, s24
	s_mul_i32 s17, s17, s24
	s_add_u32 s25, s25, 1
	s_cmp_lg_u32 s25, s16
	s_cbranch_scc1 .Lxb10_poll0
	buffer_wbl2 sc1
	s_waitcnt vmcnt(0)
	global_atomic_add v207, v245, s[14:15]

; __device__ __forceinline__ unsigned xb_ld(unsigned* p)              { return __hip_atomic_load(p, __ATOMIC_RELAXED, __HIP_MEMORY_SCOPE_AGENT); }
; __device__ __forceinline__ unsigned xb_add(unsigned* p, unsigned v) { return __hip_atomic_fetch_add(p, v, __ATOMIC_RELAXED, __HIP_MEMORY_SCOPE_AGENT); }
; #define XB_SPIN(cond, bar) do { unsigned _sp = 0; while (cond) { __builtin_amdgcn_s_sleep(1); \
;     if ((++_sp & 255u) == 0u) { if (xb_ld(&(bar)[XB_TMO])) break; if (_sp > XB_SPIN_CAP) { atomicAdd(&(bar)[XB_TMO], 1u); break; } } } } while (0)
; __device__ __forceinline__ void xcd_barrier(const XcdBarrier& b) {
;     ...
;     if (threadIdx.x == 0) {
;         unsigned* bar = b.bar;
;         __builtin_amdgcn_s_waitcnt(0);
;         unsigned nloc = b.st[0], nx = b.st[1];
;         if (nloc == 0u) { xcd_barrier_complete(bar, b.x, nloc, nx); b.st[0] = nloc; b.st[1] = nx; }
;         const unsigned old = xb_add(&bar[XB_XSUB(b.x)], 1u);
;         const unsigned gen = old / nloc;
;         if (old + 1u == (gen + 1u) * nloc) {
;             __builtin_amdgcn_fence(__ATOMIC_RELEASE, "agent");
;             asm volatile("s_waitcnt vmcnt(0)" ::: "memory");
;             const unsigned og = xb_add(&bar[XB_TOP], 1u);
;             const unsigned tg = og / nx;
;             if (og + 1u == (tg + 1u) * nx) xb_add(&bar[XB_TOPGEN], 1u);
;             else XB_SPIN(xb_ld(&bar[XB_TOPGEN]) == tg, bar);
;             __builtin_amdgcn_fence(__ATOMIC_ACQUIRE, "agent");
;             xb_add(&bar[XB_XGEN(b.x)], 1u);
;             asm volatile("s_waitcnt vmcnt(0)" ::: "memory");
;         } else {
;             XB_SPIN(xb_ld(&bar[XB_XGEN(b.x)]) == gen, bar);
;             __builtin_amdgcn_fence(__ATOMIC_ACQUIRE, "agent");
;             asm volatile("s_waitcnt vmcnt(0)" ::: "memory");
;         }
.LBB0_2377:
	v_readlane_b32 s0, v255, 56
	s_add_i32 s4, s0, 13
	s_cmp_ge_i32 s4, s87
	s_waitcnt lgkmcnt(0)
	s_barrier
	s_cbranch_scc1 .LBB0_2427
	s_waitcnt vmcnt(0)
	s_barrier
	s_mov_b64 s[0:1], exec
	v_readlane_b32 s2, v252, 34
	v_readlane_b32 s3, v252, 35
	s_and_b64 s[2:3], s[0:1], s[2:3]
	s_mov_b64 exec, s[2:3]
	s_cbranch_execz .LBB0_2426
	v_readlane_b32 s12, v253, 10
	v_readlane_b32 s13, v253, 11
	v_readlane_b32 s14, v253, 14
	v_readlane_b32 s15, v253, 15
	v_mov_b32_e32 v2, 0x20800
	ds_read_b96 v[4:6], v2
	s_nop 3
	global_atomic_add v3, v207, v245, s[12:13] sc0
	buffer_inv sc1
	s_waitcnt vmcnt(1) lgkmcnt(0)
	v_readfirstlane_b32 s16, v4
	v_readfirstlane_b32 s17, v5
	v_readfirstlane_b32 s24, v6
	v_readfirstlane_b32 s25, v3
	s_add_u32 s24, s24, 1
	v_mov_b32_e32 v6, s24
	ds_write_b32 v2, v6 offset:8
	s_mul_i32 s16, s16, s24
	s_mul_i32 s17, s17, s24
	s_add_u32 s25, s25, 1
	s_cmp_lg_u32 s25, s16
	s_cbranch_scc1 .Lxb11_poll0
	buffer_wbl2 sc1
	s_waitcnt vmcnt(0)
	global_atomic_add v207, v245, s[14:15]

; __device__ __forceinline__ unsigned xb_ld(unsigned* p)              { return __hip_atomic_load(p, __ATOMIC_RELAXED, __HIP_MEMORY_SCOPE_AGENT); }
; __device__ __forceinline__ unsigned xb_add(unsigned* p, unsigned v) { return __hip_atomic_fetch_add(p, v, __ATOMIC_RELAXED, __HIP_MEMORY_SCOPE_AGENT); }
; #define XB_SPIN(cond, bar) do { unsigned _sp = 0; while (cond) { __builtin_amdgcn_s_sleep(1); \
;     if ((++_sp & 255u) == 0u) { if (xb_ld(&(bar)[XB_TMO])) break; if (_sp > XB_SPIN_CAP) { atomicAdd(&(bar)[XB_TMO], 1u); break; } } } } while (0)
; __device__ __forceinline__ void xcd_barrier(const XcdBarrier& b) {
;     ...
;     if (threadIdx.x == 0) {
;         unsigned* bar = b.bar;
;         __builtin_amdgcn_s_waitcnt(0);
;         unsigned nloc = b.st[0], nx = b.st[1];
;         if (nloc == 0u) { xcd_barrier_complete(bar, b.x, nloc, nx); b.st[0] = nloc; b.st[1] = nx; }
;         const unsigned old = xb_add(&bar[XB_XSUB(b.x)], 1u);
;         const unsigned gen = old / nloc;
;         if (old + 1u == (gen + 1u) * nloc) {
;             __builtin_amdgcn_fence(__ATOMIC_RELEASE, "agent");
;             asm volatile("s_waitcnt vmcnt(0)" ::: "memory");
;             const unsigned og = xb_add(&bar[XB_TOP], 1u);
;             const unsigned tg = og / nx;
;             if (og + 1u == (tg + 1u) * nx) xb_add(&bar[XB_TOPGEN], 1u);
;             else XB_SPIN(xb_ld(&bar[XB_TOPGEN]) == tg, bar);
;             __builtin_amdgcn_fence(__ATOMIC_ACQUIRE, "agent");
;             xb_add(&bar[XB_XGEN(b.x)], 1u);
;             asm volatile("s_waitcnt vmcnt(0)" ::: "memory");
;         } else {
;             XB_SPIN(xb_ld(&bar[XB_XGEN(b.x)]) == gen, bar);
;             __builtin_amdgcn_fence(__ATOMIC_ACQUIRE, "agent");
;             asm volatile("s_waitcnt vmcnt(0)" ::: "memory");
;         }
.LBB0_2623:
	v_readlane_b32 s0, v255, 56
	s_add_i32 s4, s0, 14
	s_cmp_ge_i32 s4, s87
	s_cbranch_scc1 .LBB0_2673
	s_waitcnt vmcnt(0)
	s_waitcnt vmcnt(0)
	s_barrier
	s_mov_b64 s[0:1], exec
	v_readlane_b32 s2, v252, 34
	v_readlane_b32 s3, v252, 35
	s_and_b64 s[2:3], s[0:1], s[2:3]
	s_mov_b64 exec, s[2:3]
	s_cbranch_execz .LBB0_2672
	v_readlane_b32 s12, v253, 10
	v_readlane_b32 s13, v253, 11
	v_readlane_b32 s14, v253, 14
	v_readlane_b32 s15, v253, 15
	v_mov_b32_e32 v2, 0x20800
	ds_read_b96 v[4:6], v2
	s_nop 3
	global_atomic_add v3, v207, v245, s[12:13] sc0
	buffer_inv sc1
	s_waitcnt vmcnt(1) lgkmcnt(0)
	v_readfirstlane_b32 s16, v4
	v_readfirstlane_b32 s17, v5
	v_readfirstlane_b32 s24, v6
	v_readfirstlane_b32 s25, v3
	s_add_u32 s24, s24, 1
	v_mov_b32_e32 v6, s24
	ds_write_b32 v2, v6 offset:8
	s_mul_i32 s16, s16, s24
	s_mul_i32 s17, s17, s24
	s_add_u32 s25, s25, 1
	s_cmp_lg_u32 s25, s16
	s_cbranch_scc1 .Lxb12_poll0
	buffer_wbl2 sc1
	s_waitcnt vmcnt(0)
	global_atomic_add v207, v245, s[14:15]

; __device__ __forceinline__ unsigned xb_ld(unsigned* p)              { return __hip_atomic_load(p, __ATOMIC_RELAXED, __HIP_MEMORY_SCOPE_AGENT); }
; __device__ __forceinline__ unsigned xb_add(unsigned* p, unsigned v) { return __hip_atomic_fetch_add(p, v, __ATOMIC_RELAXED, __HIP_MEMORY_SCOPE_AGENT); }
; #define XB_SPIN(cond, bar) do { unsigned _sp = 0; while (cond) { __builtin_amdgcn_s_sleep(1); \
;     if ((++_sp & 255u) == 0u) { if (xb_ld(&(bar)[XB_TMO])) break; if (_sp > XB_SPIN_CAP) { atomicAdd(&(bar)[XB_TMO], 1u); break; } } } } while (0)
; __device__ __forceinline__ void xcd_barrier(const XcdBarrier& b) {
;     asm volatile("s_waitcnt vmcnt(0)" ::: "memory");
;     __syncthreads();
;     if (threadIdx.x == 0) {
;         unsigned* bar = b.bar;
;         __builtin_amdgcn_s_waitcnt(0);
;         unsigned nloc = b.st[0], nx = b.st[1];
;         if (nloc == 0u) { xcd_barrier_complete(bar, b.x, nloc, nx); b.st[0] = nloc; b.st[1] = nx; }
;         const unsigned old = xb_add(&bar[XB_XSUB(b.x)], 1u);
;         const unsigned gen = old / nloc;
;         if (old + 1u == (gen + 1u) * nloc) {
;             __builtin_amdgcn_fence(__ATOMIC_RELEASE, "agent");
;             asm volatile("s_waitcnt vmcnt(0)" ::: "memory");
;             const unsigned og = xb_add(&bar[XB_TOP], 1u);
;             const unsigned tg = og / nx;
;             if (og + 1u == (tg + 1u) * nx) xb_add(&bar[XB_TOPGEN], 1u);
;             else XB_SPIN(xb_ld(&bar[XB_TOPGEN]) == tg, bar);
;             __builtin_amdgcn_fence(__ATOMIC_ACQUIRE, "agent");
;             xb_add(&bar[XB_XGEN(b.x)], 1u);
;             asm volatile("s_waitcnt vmcnt(0)" ::: "memory");
;         } else {
;             XB_SPIN(xb_ld(&bar[XB_XGEN(b.x)]) == gen, bar);
;             __builtin_amdgcn_fence(__ATOMIC_ACQUIRE, "agent");
;             asm volatile("s_waitcnt vmcnt(0)" ::: "memory");
;         }
.LBB0_2695:
	v_readlane_b32 s12, v253, 10
	v_readlane_b32 s13, v253, 11
	v_readlane_b32 s14, v253, 14
	v_readlane_b32 s15, v253, 15
	v_mov_b32_e32 v2, 0x20800
	ds_read_b96 v[4:6], v2
	s_nop 3
	global_atomic_add v3, v207, v245, s[12:13] sc0
	buffer_inv sc1
	s_waitcnt vmcnt(1) lgkmcnt(0)
	v_readfirstlane_b32 s36, v4
	v_readfirstlane_b32 s37, v5
	v_readfirstlane_b32 s24, v6
	v_readfirstlane_b32 s25, v3
	s_add_u32 s24, s24, 1
	v_mov_b32_e32 v6, s24
	ds_write_b32 v2, v6 offset:8
	s_mul_i32 s36, s36, s24
	s_mul_i32 s37, s37, s24
	s_add_u32 s25, s25, 1
	s_cmp_lg_u32 s25, s36
	s_cbranch_scc1 .Lxb13_poll0
	buffer_wbl2 sc1
	s_waitcnt vmcnt(0)
	global_atomic_add v207, v245, s[14:15]
.Lxb13_poll0:
	s_mov_b32 s36, 0
.Lxb13_poll:
	global_load_dword v3, v207, s[14:15] sc1
	s_waitcnt vmcnt(0)
	v_readfirstlane_b32 s25, v3
	s_cmp_ge_u32 s25, s37
	s_cbranch_scc1 .Lxb13_done
	s_sleep 1
	s_add_u32 s36, s36, 1
	s_cmp_lt_u32 s36, 0x400000
	s_cbranch_scc1 .Lxb13_poll
.Lxb13_done:
	s_waitcnt vmcnt(0) lgkmcnt(0)
	s_getpc_b64 s[98:99]
